# hand-written compact P2 epilogue fast path for non-rotary sections + first-iteration vmcnt waits skipped (covered by epilogue vmcnt0), on top of sc1 stores
# speedup vs baseline: 1.0065x; 1.0065x over previous
.LBB0_238:
	ds_read_b128 v[20:23], v203
	ds_read_b128 v[34:37], v203 offset:1024
	ds_read_b128 v[38:41], v203 offset:2048
	ds_read_b128 v[208:211], v203 offset:3072
	ds_read_b128 v[212:215], v207
	ds_read_b128 v[216:219], v207 offset:1024
	ds_read_b128 v[226:229], v207 offset:2048
	ds_read_b128 v[230:233], v207 offset:3072
	s_add_u32 s28, s10, 0xfffc0080
	s_addc_u32 s29, s11, -1
	s_cmp_eq_u32 s39, 12
	s_cselect_b32 s49, s2, s29
	s_cselect_b32 s48, s3, s28
	s_cselect_b32 s47, s13, s33
	s_cselect_b32 s46, s15, s20
	v_lshl_add_u64 v[24:25], s[10:11], 0, v[174:175]
	s_add_i32 m0, s58, 0xc000
	ds_read_b128 v[234:237], v224
	ds_read_b128 v[238:241], v224 offset:1024
	ds_read_b128 v[242:245], v224 offset:2048
	ds_read_b128 v[246:249], v224 offset:3072
	ds_read_b128 v[250:253], v224 offset:4096
	ds_read_b128 v[220:223], v224 offset:5120
	ds_read_b128 v[178:181], v224 offset:6144
	ds_read_b128 v[196:199], v224 offset:7168
	global_load_lds_dwordx4 v[24:25], off
	v_lshl_add_u64 v[24:25], s[10:11], 0, v[176:177]
	s_add_i32 m0, s58, 0xe000
	s_nop 0
	global_load_lds_dwordx4 v[24:25], off
	s_cmp_eq_u32 s39, -2
	s_cbranch_scc1 .Lw1_skip
	s_waitcnt vmcnt(8)
.Lw1_skip:
	s_waitcnt lgkmcnt(0)
	s_barrier
	s_setprio 1
	s_waitcnt lgkmcnt(0)
	v_mfma_i32_16x16x64_i8 v[142:145], v[20:23], v[234:237], v[142:145]
	v_mfma_i32_16x16x64_i8 v[138:141], v[38:41], v[234:237], v[138:141]
	v_mfma_i32_16x16x64_i8 v[126:129], v[20:23], v[242:245], v[126:129]
	v_mfma_i32_16x16x64_i8 v[122:125], v[38:41], v[242:245], v[122:125]
	v_mfma_i32_16x16x64_i8 v[110:113], v[20:23], v[250:253], v[110:113]
	v_mfma_i32_16x16x64_i8 v[106:109], v[38:41], v[250:253], v[106:109]
	v_mfma_i32_16x16x64_i8 v[94:97], v[20:23], v[178:181], v[94:97]
	v_mfma_i32_16x16x64_i8 v[90:93], v[38:41], v[178:181], v[90:93]
	v_mfma_i32_16x16x64_i8 v[142:145], v[34:37], v[238:241], v[142:145]
	v_mfma_i32_16x16x64_i8 v[138:141], v[208:211], v[238:241], v[138:141]
	v_mfma_i32_16x16x64_i8 v[126:129], v[34:37], v[246:249], v[126:129]
	v_mfma_i32_16x16x64_i8 v[122:125], v[208:211], v[246:249], v[122:125]
	v_mfma_i32_16x16x64_i8 v[110:113], v[34:37], v[220:223], v[110:113]
	v_mfma_i32_16x16x64_i8 v[106:109], v[208:211], v[220:223], v[106:109]
	v_mfma_i32_16x16x64_i8 v[94:97], v[34:37], v[196:199], v[94:97]
	v_mfma_i32_16x16x64_i8 v[90:93], v[208:211], v[196:199], v[90:93]
	s_setprio 0
	s_setprio 1
	v_mfma_i32_16x16x64_i8 v[134:137], v[212:215], v[234:237], v[134:137]
	v_mfma_i32_16x16x64_i8 v[130:133], v[226:229], v[234:237], v[130:133]
	v_mfma_i32_16x16x64_i8 v[118:121], v[212:215], v[242:245], v[118:121]
	v_mfma_i32_16x16x64_i8 v[114:117], v[226:229], v[242:245], v[114:117]
	v_mfma_i32_16x16x64_i8 v[102:105], v[212:215], v[250:253], v[102:105]
	v_mfma_i32_16x16x64_i8 v[98:101], v[226:229], v[250:253], v[98:101]
	v_mfma_i32_16x16x64_i8 v[86:89], v[212:215], v[178:181], v[86:89]
	v_mfma_i32_16x16x64_i8 v[82:85], v[226:229], v[178:181], v[82:85]
	v_mfma_i32_16x16x64_i8 v[134:137], v[216:219], v[238:241], v[134:137]
	v_mfma_i32_16x16x64_i8 v[130:133], v[230:233], v[238:241], v[130:133]
	v_mfma_i32_16x16x64_i8 v[118:121], v[216:219], v[246:249], v[118:121]
	v_mfma_i32_16x16x64_i8 v[114:117], v[230:233], v[246:249], v[114:117]
	v_mfma_i32_16x16x64_i8 v[102:105], v[216:219], v[220:223], v[102:105]
	v_mfma_i32_16x16x64_i8 v[98:101], v[230:233], v[220:223], v[98:101]
	v_mfma_i32_16x16x64_i8 v[86:89], v[216:219], v[196:199], v[86:89]
	v_mfma_i32_16x16x64_i8 v[82:85], v[230:233], v[196:199], v[82:85]
	s_setprio 0
	s_barrier
	s_add_i32 s28, s80, s57
	v_lshl_add_u64 v[184:185], s[46:47], 0, v[148:149]
	s_mov_b32 m0, s28
	ds_read_b128 v[178:181], v224 offset:16384
	ds_read_b128 v[196:199], v224 offset:17408
	ds_read_b128 v[220:223], v224 offset:18432
	ds_read_b128 v[234:237], v224 offset:19456
	ds_read_b128 v[238:241], v224 offset:20480
	ds_read_b128 v[242:245], v224 offset:21504
	ds_read_b128 v[246:249], v224 offset:22528
	ds_read_b128 v[250:253], v224 offset:23552
	global_load_lds_dwordx4 v[184:185], off
	s_add_i32 m0, s28, 0x2000
	s_add_u32 s28, s46, 0x40000
	v_lshl_add_u64 v[188:189], s[46:47], 0, v[152:153]
	s_addc_u32 s29, s47, 0
	s_add_i32 s41, s81, s57
	global_load_lds_dwordx4 v[188:189], off
	v_lshl_add_u64 v[24:25], s[28:29], 0, v[148:149]
	s_mov_b32 m0, s41
	v_lshl_add_u64 v[192:193], s[48:49], 0, v[146:147]
	global_load_lds_dwordx4 v[24:25], off
	v_lshl_add_u64 v[24:25], s[28:29], 0, v[152:153]
	s_add_i32 m0, s41, 0x2000
	v_lshl_add_u64 v[200:201], s[48:49], 0, v[150:151]
	global_load_lds_dwordx4 v[24:25], off
	s_mov_b32 m0, s58
	s_nop 0
	global_load_lds_dwordx4 v[192:193], off
	s_mov_b32 m0, s59
	s_nop 0
	global_load_lds_dwordx4 v[200:201], off
	s_cmp_lg_u32 s39, -2
	s_cbranch_scc1 .Lw2_do
	s_cmp_lg_u32 s83, 1
	s_cbranch_scc1 .Lw2_skip
.Lw2_do:
	s_waitcnt vmcnt(8)
.Lw2_skip:
	s_waitcnt lgkmcnt(0)
	s_barrier
	s_setprio 1
	s_waitcnt lgkmcnt(0)
	v_mfma_i32_16x16x64_i8 v[78:81], v[20:23], v[178:181], v[78:81]
	v_mfma_i32_16x16x64_i8 v[74:77], v[38:41], v[178:181], v[74:77]
	v_mfma_i32_16x16x64_i8 v[62:65], v[20:23], v[220:223], v[62:65]
	v_mfma_i32_16x16x64_i8 v[58:61], v[38:41], v[220:223], v[58:61]
	v_mfma_i32_16x16x64_i8 v[46:49], v[20:23], v[238:241], v[46:49]
	v_mfma_i32_16x16x64_i8 v[42:45], v[38:41], v[238:241], v[42:45]
	v_mfma_i32_16x16x64_i8 v[14:17], v[20:23], v[246:249], v[14:17]
	v_mfma_i32_16x16x64_i8 v[10:13], v[38:41], v[246:249], v[10:13]
	v_mfma_i32_16x16x64_i8 v[78:81], v[34:37], v[196:199], v[78:81]
	v_mfma_i32_16x16x64_i8 v[74:77], v[208:211], v[196:199], v[74:77]
	v_mfma_i32_16x16x64_i8 v[62:65], v[34:37], v[234:237], v[62:65]
	v_mfma_i32_16x16x64_i8 v[58:61], v[208:211], v[234:237], v[58:61]
	v_mfma_i32_16x16x64_i8 v[46:49], v[34:37], v[242:245], v[46:49]
	v_mfma_i32_16x16x64_i8 v[42:45], v[208:211], v[242:245], v[42:45]
	v_mfma_i32_16x16x64_i8 v[14:17], v[34:37], v[250:253], v[14:17]
	v_mfma_i32_16x16x64_i8 v[10:13], v[208:211], v[250:253], v[10:13]
	s_setprio 0
	s_setprio 1
	v_mfma_i32_16x16x64_i8 v[50:53], v[226:229], v[220:223], v[50:53]
	v_mfma_i32_16x16x64_i8 v[30:33], v[212:215], v[238:241], v[30:33]
	v_mfma_i32_16x16x64_i8 v[24:27], v[226:229], v[238:241], v[26:29]
	v_mfma_i32_16x16x64_i8 v[6:9], v[212:215], v[246:249], v[6:9]
	v_mfma_i32_16x16x64_i8 v[2:5], v[226:229], v[246:249], v[2:5]
	v_mfma_i32_16x16x64_i8 v[20:23], v[212:215], v[178:181], v[70:73]
	v_mfma_i32_16x16x64_i8 v[34:37], v[226:229], v[178:181], v[66:69]
	v_mfma_i32_16x16x64_i8 v[38:41], v[212:215], v[220:223], v[54:57]
	v_mfma_i32_16x16x64_i8 v[50:53], v[230:233], v[234:237], v[50:53]
	v_mfma_i32_16x16x64_i8 v[30:33], v[216:219], v[242:245], v[30:33]
	v_mfma_i32_16x16x64_i8 v[24:27], v[230:233], v[242:245], v[24:27]
	v_mfma_i32_16x16x64_i8 v[6:9], v[216:219], v[250:253], v[6:9]
	v_mfma_i32_16x16x64_i8 v[2:5], v[230:233], v[250:253], v[2:5]
	v_mfma_i32_16x16x64_i8 v[20:23], v[216:219], v[196:199], v[20:23]
	v_mfma_i32_16x16x64_i8 v[34:37], v[230:233], v[196:199], v[34:37]
	v_mfma_i32_16x16x64_i8 v[38:41], v[216:219], v[234:237], v[38:41]
	s_setprio 0
	s_barrier
	s_add_i32 s41, 0, 0x18000
	v_add_u32_e32 v28, s41, v183
	s_add_i32 s50, 0, 0x1c000
	ds_read_b128 v[54:57], v28
	ds_read_b128 v[66:69], v28 offset:1024
	ds_read_b128 v[70:73], v28 offset:2048
	ds_read_b128 v[178:181], v28 offset:3072
	v_add_u32_e32 v28, s50, v183
	ds_read_b128 v[196:199], v28
	ds_read_b128 v[208:211], v28 offset:1024
	ds_read_b128 v[212:215], v28 offset:2048
	ds_read_b128 v[216:219], v28 offset:3072
	s_add_u32 s28, s48, 0x40000
	s_addc_u32 s29, s49, 0
	s_mov_b32 m0, s60
	v_lshl_add_u64 v[28:29], s[28:29], 0, v[146:147]
	ds_read_b128 v[220:223], v224 offset:32768
	ds_read_b128 v[226:229], v224 offset:33792
	ds_read_b128 v[230:233], v224 offset:34816
	ds_read_b128 v[234:237], v224 offset:35840
	ds_read_b128 v[238:241], v224 offset:36864
	ds_read_b128 v[242:245], v224 offset:37888
	ds_read_b128 v[246:249], v224 offset:38912
	ds_read_b128 v[250:253], v224 offset:39936
	global_load_lds_dwordx4 v[28:29], off
	v_lshl_add_u64 v[28:29], s[28:29], 0, v[150:151]
	s_mov_b32 m0, s61
	s_nop 0
	global_load_lds_dwordx4 v[28:29], off
	s_waitcnt vmcnt(8)
	s_waitcnt lgkmcnt(0)
	s_barrier
	s_setprio 1
	s_waitcnt lgkmcnt(0)
	v_mfma_i32_16x16x64_i8 v[142:145], v[54:57], v[220:223], v[142:145]
	v_mfma_i32_16x16x64_i8 v[138:141], v[70:73], v[220:223], v[138:141]
	v_mfma_i32_16x16x64_i8 v[126:129], v[54:57], v[230:233], v[126:129]
	v_mfma_i32_16x16x64_i8 v[122:125], v[70:73], v[230:233], v[122:125]
	v_mfma_i32_16x16x64_i8 v[110:113], v[54:57], v[238:241], v[110:113]
	v_mfma_i32_16x16x64_i8 v[106:109], v[70:73], v[238:241], v[106:109]
	v_mfma_i32_16x16x64_i8 v[94:97], v[54:57], v[246:249], v[94:97]
	v_mfma_i32_16x16x64_i8 v[90:93], v[70:73], v[246:249], v[90:93]
	v_mfma_i32_16x16x64_i8 v[142:145], v[66:69], v[226:229], v[142:145]
	v_mfma_i32_16x16x64_i8 v[138:141], v[178:181], v[226:229], v[138:141]
	v_mfma_i32_16x16x64_i8 v[126:129], v[66:69], v[234:237], v[126:129]
	v_mfma_i32_16x16x64_i8 v[122:125], v[178:181], v[234:237], v[122:125]
	v_mfma_i32_16x16x64_i8 v[110:113], v[66:69], v[242:245], v[110:113]
	v_mfma_i32_16x16x64_i8 v[106:109], v[178:181], v[242:245], v[106:109]
	v_mfma_i32_16x16x64_i8 v[94:97], v[66:69], v[250:253], v[94:97]
	v_mfma_i32_16x16x64_i8 v[90:93], v[178:181], v[250:253], v[90:93]
	s_setprio 0
	s_setprio 1
	v_mfma_i32_16x16x64_i8 v[134:137], v[196:199], v[220:223], v[134:137]
	v_mfma_i32_16x16x64_i8 v[130:133], v[212:215], v[220:223], v[130:133]
	v_mfma_i32_16x16x64_i8 v[118:121], v[196:199], v[230:233], v[118:121]
	v_mfma_i32_16x16x64_i8 v[114:117], v[212:215], v[230:233], v[114:117]
	v_mfma_i32_16x16x64_i8 v[102:105], v[196:199], v[238:241], v[102:105]
	v_mfma_i32_16x16x64_i8 v[98:101], v[212:215], v[238:241], v[98:101]
	v_mfma_i32_16x16x64_i8 v[86:89], v[196:199], v[246:249], v[86:89]
	v_mfma_i32_16x16x64_i8 v[82:85], v[212:215], v[246:249], v[82:85]
	v_mfma_i32_16x16x64_i8 v[134:137], v[208:211], v[226:229], v[134:137]
	v_mfma_i32_16x16x64_i8 v[130:133], v[216:219], v[226:229], v[130:133]
	v_mfma_i32_16x16x64_i8 v[118:121], v[208:211], v[234:237], v[118:121]
	v_mfma_i32_16x16x64_i8 v[114:117], v[216:219], v[234:237], v[114:117]
	v_mfma_i32_16x16x64_i8 v[102:105], v[208:211], v[242:245], v[102:105]
	v_mfma_i32_16x16x64_i8 v[98:101], v[216:219], v[242:245], v[98:101]
	v_mfma_i32_16x16x64_i8 v[86:89], v[208:211], v[250:253], v[86:89]
	v_mfma_i32_16x16x64_i8 v[82:85], v[216:219], v[250:253], v[82:85]
	s_setprio 0
	s_barrier
	s_add_i32 s28, s41, s57
	v_lshl_add_u64 v[28:29], v[184:185], 0, s[24:25]
	s_mov_b32 m0, s28
	ds_read_b128 v[220:223], v224 offset:49152
	ds_read_b128 v[226:229], v224 offset:50176
	ds_read_b128 v[230:233], v224 offset:51200
	ds_read_b128 v[234:237], v224 offset:52224
	ds_read_b128 v[238:241], v224 offset:53248
	ds_read_b128 v[242:245], v224 offset:54272
	ds_read_b128 v[246:249], v224 offset:55296
	ds_read_b128 v[250:253], v224 offset:56320
	global_load_lds_dwordx4 v[28:29], off
	s_add_i32 m0, s28, 0x2000
	s_add_u32 s28, s46, 0x40080
	v_lshl_add_u64 v[28:29], v[188:189], 0, s[24:25]
	s_addc_u32 s29, s47, 0
	s_add_i32 s41, s50, s57
	global_load_lds_dwordx4 v[28:29], off
	v_lshl_add_u64 v[28:29], s[28:29], 0, v[148:149]
	s_mov_b32 m0, s41
	s_nop 0
	global_load_lds_dwordx4 v[28:29], off
	v_lshl_add_u64 v[28:29], s[28:29], 0, v[152:153]
	s_add_i32 m0, s41, 0x2000
	s_nop 0
	global_load_lds_dwordx4 v[28:29], off
	v_lshl_add_u64 v[28:29], v[192:193], 0, s[24:25]
	s_mov_b32 m0, s64
	s_nop 0
	global_load_lds_dwordx4 v[28:29], off
	v_lshl_add_u64 v[28:29], v[200:201], 0, s[24:25]
	s_mov_b32 m0, s65
	s_nop 0
	global_load_lds_dwordx4 v[28:29], off
	s_waitcnt vmcnt(8)
	s_waitcnt lgkmcnt(0)
	s_barrier
	s_setprio 1
	s_waitcnt lgkmcnt(0)
	v_mfma_i32_16x16x64_i8 v[78:81], v[54:57], v[220:223], v[78:81]
	v_mfma_i32_16x16x64_i8 v[74:77], v[70:73], v[220:223], v[74:77]
	v_mfma_i32_16x16x64_i8 v[62:65], v[54:57], v[230:233], v[62:65]
	v_mfma_i32_16x16x64_i8 v[58:61], v[70:73], v[230:233], v[58:61]
	v_mfma_i32_16x16x64_i8 v[46:49], v[54:57], v[238:241], v[46:49]
	v_mfma_i32_16x16x64_i8 v[42:45], v[70:73], v[238:241], v[42:45]
	v_mfma_i32_16x16x64_i8 v[14:17], v[54:57], v[246:249], v[14:17]
	v_mfma_i32_16x16x64_i8 v[10:13], v[70:73], v[246:249], v[10:13]
	v_mfma_i32_16x16x64_i8 v[78:81], v[66:69], v[226:229], v[78:81]
	v_mfma_i32_16x16x64_i8 v[74:77], v[178:181], v[226:229], v[74:77]
	v_mfma_i32_16x16x64_i8 v[62:65], v[66:69], v[234:237], v[62:65]
	v_mfma_i32_16x16x64_i8 v[58:61], v[178:181], v[234:237], v[58:61]
	v_mfma_i32_16x16x64_i8 v[46:49], v[66:69], v[242:245], v[46:49]
	v_mfma_i32_16x16x64_i8 v[42:45], v[178:181], v[242:245], v[42:45]
	v_mfma_i32_16x16x64_i8 v[14:17], v[66:69], v[250:253], v[14:17]
	v_mfma_i32_16x16x64_i8 v[10:13], v[178:181], v[250:253], v[10:13]
	s_setprio 0
	s_setprio 1
	v_mfma_i32_16x16x64_i8 v[20:23], v[196:199], v[220:223], v[20:23]
	v_mfma_i32_16x16x64_i8 v[70:73], v[208:211], v[226:229], v[20:23]
	v_mfma_i32_16x16x64_i8 v[20:23], v[212:215], v[220:223], v[34:37]
	v_mfma_i32_16x16x64_i8 v[66:69], v[216:219], v[226:229], v[20:23]
	v_mfma_i32_16x16x64_i8 v[20:23], v[196:199], v[230:233], v[38:41]
	v_mfma_i32_16x16x64_i8 v[54:57], v[208:211], v[234:237], v[20:23]
	v_mfma_i32_16x16x64_i8 v[20:23], v[212:215], v[230:233], v[50:53]
	v_mfma_i32_16x16x64_i8 v[50:53], v[216:219], v[234:237], v[20:23]
	v_mfma_i32_16x16x64_i8 v[20:23], v[196:199], v[238:241], v[30:33]
	v_mfma_i32_16x16x64_i8 v[30:33], v[208:211], v[242:245], v[20:23]
	v_mfma_i32_16x16x64_i8 v[20:23], v[212:215], v[238:241], v[24:27]
	v_mfma_i32_16x16x64_i8 v[6:9], v[196:199], v[246:249], v[6:9]
	v_mfma_i32_16x16x64_i8 v[2:5], v[212:215], v[246:249], v[2:5]
	v_mfma_i32_16x16x64_i8 v[26:29], v[216:219], v[242:245], v[20:23]
	v_mfma_i32_16x16x64_i8 v[6:9], v[208:211], v[250:253], v[6:9]
	v_mfma_i32_16x16x64_i8 v[2:5], v[216:219], v[250:253], v[2:5]
	s_setprio 0
	s_barrier
	s_add_i32 s39, s39, 2
	s_add_u32 s10, s10, 0x100
	s_addc_u32 s11, s11, 0
	s_add_u32 s20, s20, 0x100
	s_addc_u32 s33, s33, 0
	s_cmp_gt_u32 s39, 13
	s_cbranch_scc0 .LBB0_238
	s_and_b64 vcc, exec, s[26:27]
	s_cbranch_vccz .LBB0_241
	s_barrier
.LBB0_241:
	s_waitcnt vmcnt(0)
	ds_write_b32 v187, v18
	s_and_saveexec_b64 s[10:11], s[0:1]
	v_cvt_f32_i32_e32 v18, v19
	ds_write_b32 v187, v18 offset:2048
	s_or_b64 exec, exec, s[10:11]
	s_ashr_i32 s39, s12, 3
	s_waitcnt lgkmcnt(0)
	s_barrier
	s_cmp_gt_i32 s39, 1
	s_cbranch_scc1 .Lfast_epi
	s_cmp_lt_i32 s39, 2
	ds_read_b32 v212, v191
	s_cselect_b64 s[2:3], -1, 0
	s_and_b64 s[2:3], s[30:31], s[2:3]
	v_cndmask_b32_e64 v18, 0, 1, s[2:3]
	v_mov_b32_e32 v206, 0
	v_cmp_ne_u32_e64 s[10:11], 1, v18
	s_andn2_b64 vcc, exec, s[2:3]
	v_mov_b32_e32 v210, 0
	s_cbranch_vccnz .LBB0_245
	ds_read_b32 v210, v191 offset:2048

.LBB0_453:
	s_andn2_b64 vcc, exec, s[8:9]
	s_mov_b64 s[8:9], -1
	global_store_dwordx4 v[6:7], v[2:5], off sc1
	s_cbranch_vccnz .LBB0_234
	s_branch .Lpre_next
.Lfast_epi:
	ds_read_b32 v208, v191
	ds_read_b32 v210, v191 offset:64
	ds_read_b32 v212, v191 offset:128
	ds_read_b32 v214, v191 offset:192
	ds_read_b32 v178, v191 offset:512
	ds_read_b32 v180, v191 offset:576
	ds_read_b32 v196, v191 offset:640
	ds_read_b32 v198, v191 offset:704
	ds_read_b128 v[216:219], v195
	ds_read_b128 v[220:223], v195 offset:16
	ds_read_b128 v[226:229], v195 offset:512
	ds_read_b128 v[230:233], v195 offset:528
	v_and_b32_e32 v238, 15, v0
	v_mov_b32_e32 v239, 0
	s_mov_b32 s47, 0
	s_mov_b32 s49, 0
	s_mov_b32 s51, 0
	s_cmp_eq_u32 s39, 2
	s_cbranch_scc1 .Lfast_kvaddr
	s_lshl_b32 s2, s14, 8
	s_add_i32 s2, s2, s62
	v_readlane_b32 s28, v255, 4
	v_readlane_b32 s29, v255, 5
	v_or_b32_e32 v238, s2, v238
	v_mul_lo_u32 v238, v238, s82
	v_lshl_or_b32 v240, s12, 8, v157
	v_lshl_add_u32 v238, v240, 1, v238
	s_mov_b32 s46, 0x90000
	s_mov_b32 s48, 0x2d0000
	s_movk_i32 s50, 0x100
	s_branch .Lfast_addr_done
.Lfast_kvaddr:
	s_lshr_b32 s2, s14, 3
	s_lshl_b32 s2, s2, 4
	s_and_b32 s3, s12, 7
	s_lshl_b32 s3, s3, 1
	s_or_b32 s2, s2, s3
	s_lshl_b32 s2, s2, 19
	s_add_u32 s28, s78, 0x4000000
	s_addc_u32 s29, s79, 0
	s_add_u32 s28, s28, s2
	s_addc_u32 s29, s29, 0
	s_and_b32 s2, s14, 7
	s_lshl_b32 s2, s2, 8
	s_add_i32 s2, s2, s62
	v_or_b32_e32 v238, s2, v238
	v_lshlrev_b32_e32 v238, 8, v238
	v_lshl_add_u32 v238, v157, 1, v238
	s_movk_i32 s46, 0x1000
	s_movk_i32 s48, 0x5000
	s_mov_b32 s50, 0x80000
.Lfast_addr_done:
	s_nop 1
	v_lshl_add_u64 v[234:235], s[28:29], 0, v[238:239]
	s_cmp_gt_i32 s39, 6
	s_cbranch_scc1 .Lfast_sigm
	s_cmp_eq_u32 s39, 3
	s_cbranch_scc1 .Lfast_silu
	s_cmp_eq_u32 s39, 6
	s_cbranch_scc1 .Lfast_silu
	v_lshl_add_u64 v[236:237], v[234:235], 0, s[50:51]
	v_cvt_f32_i32_e32 v142, v142
	v_cvt_f32_i32_e32 v143, v143
	v_cvt_f32_i32_e32 v144, v144
	v_cvt_f32_i32_e32 v145, v145
	v_cvt_f32_i32_e32 v138, v138
	v_cvt_f32_i32_e32 v139, v139
	v_cvt_f32_i32_e32 v140, v140
	v_cvt_f32_i32_e32 v141, v141
	s_waitcnt lgkmcnt(0)
	v_pk_mul_f32 v[142:143], v[142:143], v[208:209] op_sel_hi:[1,0]
	v_pk_mul_f32 v[144:145], v[144:145], v[208:209] op_sel_hi:[1,0]
	v_pk_mul_f32 v[138:139], v[138:139], v[208:209] op_sel_hi:[1,0]
	v_pk_mul_f32 v[140:141], v[140:141], v[208:209] op_sel_hi:[1,0]
	v_pk_mul_f32 v[142:143], v[142:143], v[216:217]
	v_pk_mul_f32 v[144:145], v[144:145], v[218:219]
	v_pk_mul_f32 v[138:139], v[138:139], v[220:221]
	v_pk_mul_f32 v[140:141], v[140:141], v[222:223]
	v_cvt_pk_bf16_f32 v142, v142, v143
	v_cvt_pk_bf16_f32 v143, v144, v145
	v_cvt_pk_bf16_f32 v144, v138, v139
	v_cvt_pk_bf16_f32 v145, v140, v141
	global_store_dwordx4 v[234:235], v[142:145], off sc1
	v_cvt_f32_i32_e32 v134, v134
	v_cvt_f32_i32_e32 v135, v135
	v_cvt_f32_i32_e32 v136, v136
	v_cvt_f32_i32_e32 v137, v137
	v_cvt_f32_i32_e32 v130, v130
	v_cvt_f32_i32_e32 v131, v131
	v_cvt_f32_i32_e32 v132, v132
	v_cvt_f32_i32_e32 v133, v133
	v_pk_mul_f32 v[134:135], v[134:135], v[208:209] op_sel_hi:[1,0]
	v_pk_mul_f32 v[136:137], v[136:137], v[208:209] op_sel_hi:[1,0]
	v_pk_mul_f32 v[130:131], v[130:131], v[208:209] op_sel_hi:[1,0]
	v_pk_mul_f32 v[132:133], v[132:133], v[208:209] op_sel_hi:[1,0]
	v_pk_mul_f32 v[134:135], v[134:135], v[226:227]
	v_pk_mul_f32 v[136:137], v[136:137], v[228:229]
	v_pk_mul_f32 v[130:131], v[130:131], v[230:231]
	v_pk_mul_f32 v[132:133], v[132:133], v[232:233]
	v_cvt_pk_bf16_f32 v134, v134, v135
	v_cvt_pk_bf16_f32 v135, v136, v137
	v_cvt_pk_bf16_f32 v136, v130, v131
	v_cvt_pk_bf16_f32 v137, v132, v133
	global_store_dwordx4 v[236:237], v[134:137], off sc1
	v_lshl_add_u64 v[234:235], v[234:235], 0, s[46:47]
	v_lshl_add_u64 v[236:237], v[234:235], 0, s[50:51]
	v_cvt_f32_i32_e32 v126, v126
	v_cvt_f32_i32_e32 v127, v127
	v_cvt_f32_i32_e32 v128, v128
	v_cvt_f32_i32_e32 v129, v129
	v_cvt_f32_i32_e32 v122, v122
	v_cvt_f32_i32_e32 v123, v123
	v_cvt_f32_i32_e32 v124, v124
	v_cvt_f32_i32_e32 v125, v125
	v_pk_mul_f32 v[126:127], v[126:127], v[210:211] op_sel_hi:[1,0]
	v_pk_mul_f32 v[128:129], v[128:129], v[210:211] op_sel_hi:[1,0]
	v_pk_mul_f32 v[122:123], v[122:123], v[210:211] op_sel_hi:[1,0]
	v_pk_mul_f32 v[124:125], v[124:125], v[210:211] op_sel_hi:[1,0]
	v_pk_mul_f32 v[126:127], v[126:127], v[216:217]
	v_pk_mul_f32 v[128:129], v[128:129], v[218:219]
	v_pk_mul_f32 v[122:123], v[122:123], v[220:221]
	v_pk_mul_f32 v[124:125], v[124:125], v[222:223]
	v_cvt_pk_bf16_f32 v126, v126, v127
	v_cvt_pk_bf16_f32 v127, v128, v129
	v_cvt_pk_bf16_f32 v128, v122, v123
	v_cvt_pk_bf16_f32 v129, v124, v125
	global_store_dwordx4 v[234:235], v[126:129], off sc1
	v_cvt_f32_i32_e32 v118, v118
	v_cvt_f32_i32_e32 v119, v119
	v_cvt_f32_i32_e32 v120, v120
	v_cvt_f32_i32_e32 v121, v121
	v_cvt_f32_i32_e32 v114, v114
	v_cvt_f32_i32_e32 v115, v115
	v_cvt_f32_i32_e32 v116, v116
	v_cvt_f32_i32_e32 v117, v117
	v_pk_mul_f32 v[118:119], v[118:119], v[210:211] op_sel_hi:[1,0]
	v_pk_mul_f32 v[120:121], v[120:121], v[210:211] op_sel_hi:[1,0]
	v_pk_mul_f32 v[114:115], v[114:115], v[210:211] op_sel_hi:[1,0]
	v_pk_mul_f32 v[116:117], v[116:117], v[210:211] op_sel_hi:[1,0]
	v_pk_mul_f32 v[118:119], v[118:119], v[226:227]
	v_pk_mul_f32 v[120:121], v[120:121], v[228:229]
	v_pk_mul_f32 v[114:115], v[114:115], v[230:231]
	v_pk_mul_f32 v[116:117], v[116:117], v[232:233]
	v_cvt_pk_bf16_f32 v118, v118, v119
	v_cvt_pk_bf16_f32 v119, v120, v121
	v_cvt_pk_bf16_f32 v120, v114, v115
	v_cvt_pk_bf16_f32 v121, v116, v117
	global_store_dwordx4 v[236:237], v[118:121], off sc1
	v_lshl_add_u64 v[234:235], v[234:235], 0, s[46:47]
	v_lshl_add_u64 v[236:237], v[234:235], 0, s[50:51]
	v_cvt_f32_i32_e32 v110, v110
	v_cvt_f32_i32_e32 v111, v111
	v_cvt_f32_i32_e32 v112, v112
	v_cvt_f32_i32_e32 v113, v113
	v_cvt_f32_i32_e32 v106, v106
	v_cvt_f32_i32_e32 v107, v107
	v_cvt_f32_i32_e32 v108, v108
	v_cvt_f32_i32_e32 v109, v109
	v_pk_mul_f32 v[110:111], v[110:111], v[212:213] op_sel_hi:[1,0]
	v_pk_mul_f32 v[112:113], v[112:113], v[212:213] op_sel_hi:[1,0]
	v_pk_mul_f32 v[106:107], v[106:107], v[212:213] op_sel_hi:[1,0]
	v_pk_mul_f32 v[108:109], v[108:109], v[212:213] op_sel_hi:[1,0]
	v_pk_mul_f32 v[110:111], v[110:111], v[216:217]
	v_pk_mul_f32 v[112:113], v[112:113], v[218:219]
	v_pk_mul_f32 v[106:107], v[106:107], v[220:221]
	v_pk_mul_f32 v[108:109], v[108:109], v[222:223]
	v_cvt_pk_bf16_f32 v110, v110, v111
	v_cvt_pk_bf16_f32 v111, v112, v113
	v_cvt_pk_bf16_f32 v112, v106, v107
	v_cvt_pk_bf16_f32 v113, v108, v109
	global_store_dwordx4 v[234:235], v[110:113], off sc1
	v_cvt_f32_i32_e32 v102, v102
	v_cvt_f32_i32_e32 v103, v103
	v_cvt_f32_i32_e32 v104, v104
	v_cvt_f32_i32_e32 v105, v105
	v_cvt_f32_i32_e32 v98, v98
	v_cvt_f32_i32_e32 v99, v99
	v_cvt_f32_i32_e32 v100, v100
	v_cvt_f32_i32_e32 v101, v101
	v_pk_mul_f32 v[102:103], v[102:103], v[212:213] op_sel_hi:[1,0]
	v_pk_mul_f32 v[104:105], v[104:105], v[212:213] op_sel_hi:[1,0]
	v_pk_mul_f32 v[98:99], v[98:99], v[212:213] op_sel_hi:[1,0]
	v_pk_mul_f32 v[100:101], v[100:101], v[212:213] op_sel_hi:[1,0]
	v_pk_mul_f32 v[102:103], v[102:103], v[226:227]
	v_pk_mul_f32 v[104:105], v[104:105], v[228:229]
	v_pk_mul_f32 v[98:99], v[98:99], v[230:231]
	v_pk_mul_f32 v[100:101], v[100:101], v[232:233]
	v_cvt_pk_bf16_f32 v102, v102, v103
	v_cvt_pk_bf16_f32 v103, v104, v105
	v_cvt_pk_bf16_f32 v104, v98, v99
	v_cvt_pk_bf16_f32 v105, v100, v101
	global_store_dwordx4 v[236:237], v[102:105], off sc1
	v_lshl_add_u64 v[234:235], v[234:235], 0, s[46:47]
	v_lshl_add_u64 v[236:237], v[234:235], 0, s[50:51]
	v_cvt_f32_i32_e32 v94, v94
	v_cvt_f32_i32_e32 v95, v95
	v_cvt_f32_i32_e32 v96, v96
	v_cvt_f32_i32_e32 v97, v97
	v_cvt_f32_i32_e32 v90, v90
	v_cvt_f32_i32_e32 v91, v91
	v_cvt_f32_i32_e32 v92, v92
	v_cvt_f32_i32_e32 v93, v93
	v_pk_mul_f32 v[94:95], v[94:95], v[214:215] op_sel_hi:[1,0]
	v_pk_mul_f32 v[96:97], v[96:97], v[214:215] op_sel_hi:[1,0]
	v_pk_mul_f32 v[90:91], v[90:91], v[214:215] op_sel_hi:[1,0]
	v_pk_mul_f32 v[92:93], v[92:93], v[214:215] op_sel_hi:[1,0]
	v_pk_mul_f32 v[94:95], v[94:95], v[216:217]
	v_pk_mul_f32 v[96:97], v[96:97], v[218:219]
	v_pk_mul_f32 v[90:91], v[90:91], v[220:221]
	v_pk_mul_f32 v[92:93], v[92:93], v[222:223]
	v_cvt_pk_bf16_f32 v94, v94, v95
	v_cvt_pk_bf16_f32 v95, v96, v97
	v_cvt_pk_bf16_f32 v96, v90, v91
	v_cvt_pk_bf16_f32 v97, v92, v93
	global_store_dwordx4 v[234:235], v[94:97], off sc1
	v_cvt_f32_i32_e32 v86, v86
	v_cvt_f32_i32_e32 v87, v87
	v_cvt_f32_i32_e32 v88, v88
	v_cvt_f32_i32_e32 v89, v89
	v_cvt_f32_i32_e32 v82, v82
	v_cvt_f32_i32_e32 v83, v83
	v_cvt_f32_i32_e32 v84, v84
	v_cvt_f32_i32_e32 v85, v85
	v_pk_mul_f32 v[86:87], v[86:87], v[214:215] op_sel_hi:[1,0]
	v_pk_mul_f32 v[88:89], v[88:89], v[214:215] op_sel_hi:[1,0]
	v_pk_mul_f32 v[82:83], v[82:83], v[214:215] op_sel_hi:[1,0]
	v_pk_mul_f32 v[84:85], v[84:85], v[214:215] op_sel_hi:[1,0]
	v_pk_mul_f32 v[86:87], v[86:87], v[226:227]
	v_pk_mul_f32 v[88:89], v[88:89], v[228:229]
	v_pk_mul_f32 v[82:83], v[82:83], v[230:231]
	v_pk_mul_f32 v[84:85], v[84:85], v[232:233]
	v_cvt_pk_bf16_f32 v86, v86, v87
	v_cvt_pk_bf16_f32 v87, v88, v89
	v_cvt_pk_bf16_f32 v88, v82, v83
	v_cvt_pk_bf16_f32 v89, v84, v85
	global_store_dwordx4 v[236:237], v[86:89], off sc1
	v_lshl_add_u64 v[234:235], v[234:235], 0, s[48:49]
	v_lshl_add_u64 v[236:237], v[234:235], 0, s[50:51]
	v_cvt_f32_i32_e32 v78, v78
	v_cvt_f32_i32_e32 v79, v79
	v_cvt_f32_i32_e32 v80, v80
	v_cvt_f32_i32_e32 v81, v81
	v_cvt_f32_i32_e32 v74, v74
	v_cvt_f32_i32_e32 v75, v75
	v_cvt_f32_i32_e32 v76, v76
	v_cvt_f32_i32_e32 v77, v77
	v_pk_mul_f32 v[78:79], v[78:79], v[178:179] op_sel_hi:[1,0]
	v_pk_mul_f32 v[80:81], v[80:81], v[178:179] op_sel_hi:[1,0]
	v_pk_mul_f32 v[74:75], v[74:75], v[178:179] op_sel_hi:[1,0]
	v_pk_mul_f32 v[76:77], v[76:77], v[178:179] op_sel_hi:[1,0]
	v_pk_mul_f32 v[78:79], v[78:79], v[216:217]
	v_pk_mul_f32 v[80:81], v[80:81], v[218:219]
	v_pk_mul_f32 v[74:75], v[74:75], v[220:221]
	v_pk_mul_f32 v[76:77], v[76:77], v[222:223]
	v_cvt_pk_bf16_f32 v78, v78, v79
	v_cvt_pk_bf16_f32 v79, v80, v81
	v_cvt_pk_bf16_f32 v80, v74, v75
	v_cvt_pk_bf16_f32 v81, v76, v77
	global_store_dwordx4 v[234:235], v[78:81], off sc1
	v_cvt_f32_i32_e32 v70, v70
	v_cvt_f32_i32_e32 v71, v71
	v_cvt_f32_i32_e32 v72, v72
	v_cvt_f32_i32_e32 v73, v73
	v_cvt_f32_i32_e32 v66, v66
	v_cvt_f32_i32_e32 v67, v67
	v_cvt_f32_i32_e32 v68, v68
	v_cvt_f32_i32_e32 v69, v69
	v_pk_mul_f32 v[70:71], v[70:71], v[178:179] op_sel_hi:[1,0]
	v_pk_mul_f32 v[72:73], v[72:73], v[178:179] op_sel_hi:[1,0]
	v_pk_mul_f32 v[66:67], v[66:67], v[178:179] op_sel_hi:[1,0]
	v_pk_mul_f32 v[68:69], v[68:69], v[178:179] op_sel_hi:[1,0]
	v_pk_mul_f32 v[70:71], v[70:71], v[226:227]
	v_pk_mul_f32 v[72:73], v[72:73], v[228:229]
	v_pk_mul_f32 v[66:67], v[66:67], v[230:231]
	v_pk_mul_f32 v[68:69], v[68:69], v[232:233]
	v_cvt_pk_bf16_f32 v70, v70, v71
	v_cvt_pk_bf16_f32 v71, v72, v73
	v_cvt_pk_bf16_f32 v72, v66, v67
	v_cvt_pk_bf16_f32 v73, v68, v69
	global_store_dwordx4 v[236:237], v[70:73], off sc1
	v_lshl_add_u64 v[234:235], v[234:235], 0, s[46:47]
	v_lshl_add_u64 v[236:237], v[234:235], 0, s[50:51]
	v_cvt_f32_i32_e32 v62, v62
	v_cvt_f32_i32_e32 v63, v63
	v_cvt_f32_i32_e32 v64, v64
	v_cvt_f32_i32_e32 v65, v65
	v_cvt_f32_i32_e32 v58, v58
	v_cvt_f32_i32_e32 v59, v59
	v_cvt_f32_i32_e32 v60, v60
	v_cvt_f32_i32_e32 v61, v61
	v_pk_mul_f32 v[62:63], v[62:63], v[180:181] op_sel_hi:[1,0]
	v_pk_mul_f32 v[64:65], v[64:65], v[180:181] op_sel_hi:[1,0]
	v_pk_mul_f32 v[58:59], v[58:59], v[180:181] op_sel_hi:[1,0]
	v_pk_mul_f32 v[60:61], v[60:61], v[180:181] op_sel_hi:[1,0]
	v_pk_mul_f32 v[62:63], v[62:63], v[216:217]
	v_pk_mul_f32 v[64:65], v[64:65], v[218:219]
	v_pk_mul_f32 v[58:59], v[58:59], v[220:221]
	v_pk_mul_f32 v[60:61], v[60:61], v[222:223]
	v_cvt_pk_bf16_f32 v62, v62, v63
	v_cvt_pk_bf16_f32 v63, v64, v65
	v_cvt_pk_bf16_f32 v64, v58, v59
	v_cvt_pk_bf16_f32 v65, v60, v61
	global_store_dwordx4 v[234:235], v[62:65], off sc1
	v_cvt_f32_i32_e32 v54, v54
	v_cvt_f32_i32_e32 v55, v55
	v_cvt_f32_i32_e32 v56, v56
	v_cvt_f32_i32_e32 v57, v57
	v_cvt_f32_i32_e32 v50, v50
	v_cvt_f32_i32_e32 v51, v51
	v_cvt_f32_i32_e32 v52, v52
	v_cvt_f32_i32_e32 v53, v53
	v_pk_mul_f32 v[54:55], v[54:55], v[180:181] op_sel_hi:[1,0]
	v_pk_mul_f32 v[56:57], v[56:57], v[180:181] op_sel_hi:[1,0]
	v_pk_mul_f32 v[50:51], v[50:51], v[180:181] op_sel_hi:[1,0]
	v_pk_mul_f32 v[52:53], v[52:53], v[180:181] op_sel_hi:[1,0]
	v_pk_mul_f32 v[54:55], v[54:55], v[226:227]
	v_pk_mul_f32 v[56:57], v[56:57], v[228:229]
	v_pk_mul_f32 v[50:51], v[50:51], v[230:231]
	v_pk_mul_f32 v[52:53], v[52:53], v[232:233]
	v_cvt_pk_bf16_f32 v54, v54, v55
	v_cvt_pk_bf16_f32 v55, v56, v57
	v_cvt_pk_bf16_f32 v56, v50, v51
	v_cvt_pk_bf16_f32 v57, v52, v53
	global_store_dwordx4 v[236:237], v[54:57], off sc1
	v_lshl_add_u64 v[234:235], v[234:235], 0, s[46:47]
	v_lshl_add_u64 v[236:237], v[234:235], 0, s[50:51]
	v_cvt_f32_i32_e32 v46, v46
	v_cvt_f32_i32_e32 v47, v47
	v_cvt_f32_i32_e32 v48, v48
	v_cvt_f32_i32_e32 v49, v49
	v_cvt_f32_i32_e32 v42, v42
	v_cvt_f32_i32_e32 v43, v43
	v_cvt_f32_i32_e32 v44, v44
	v_cvt_f32_i32_e32 v45, v45
	v_pk_mul_f32 v[46:47], v[46:47], v[196:197] op_sel_hi:[1,0]
	v_pk_mul_f32 v[48:49], v[48:49], v[196:197] op_sel_hi:[1,0]
	v_pk_mul_f32 v[42:43], v[42:43], v[196:197] op_sel_hi:[1,0]
	v_pk_mul_f32 v[44:45], v[44:45], v[196:197] op_sel_hi:[1,0]
	v_pk_mul_f32 v[46:47], v[46:47], v[216:217]
	v_pk_mul_f32 v[48:49], v[48:49], v[218:219]
	v_pk_mul_f32 v[42:43], v[42:43], v[220:221]
	v_pk_mul_f32 v[44:45], v[44:45], v[222:223]
	v_cvt_pk_bf16_f32 v46, v46, v47
	v_cvt_pk_bf16_f32 v47, v48, v49
	v_cvt_pk_bf16_f32 v48, v42, v43
	v_cvt_pk_bf16_f32 v49, v44, v45
	global_store_dwordx4 v[234:235], v[46:49], off sc1
	v_cvt_f32_i32_e32 v30, v30
	v_cvt_f32_i32_e32 v31, v31
	v_cvt_f32_i32_e32 v32, v32
	v_cvt_f32_i32_e32 v33, v33
	v_cvt_f32_i32_e32 v26, v26
	v_cvt_f32_i32_e32 v27, v27
	v_cvt_f32_i32_e32 v28, v28
	v_cvt_f32_i32_e32 v29, v29
	v_pk_mul_f32 v[30:31], v[30:31], v[196:197] op_sel_hi:[1,0]
	v_pk_mul_f32 v[32:33], v[32:33], v[196:197] op_sel_hi:[1,0]
	v_pk_mul_f32 v[26:27], v[26:27], v[196:197] op_sel_hi:[1,0]
	v_pk_mul_f32 v[28:29], v[28:29], v[196:197] op_sel_hi:[1,0]
	v_pk_mul_f32 v[30:31], v[30:31], v[226:227]
	v_pk_mul_f32 v[32:33], v[32:33], v[228:229]
	v_pk_mul_f32 v[26:27], v[26:27], v[230:231]
	v_pk_mul_f32 v[28:29], v[28:29], v[232:233]
	v_cvt_pk_bf16_f32 v30, v30, v31
	v_cvt_pk_bf16_f32 v31, v32, v33
	v_cvt_pk_bf16_f32 v32, v26, v27
	v_cvt_pk_bf16_f32 v33, v28, v29
	global_store_dwordx4 v[236:237], v[30:33], off sc1
	v_lshl_add_u64 v[234:235], v[234:235], 0, s[46:47]
	v_lshl_add_u64 v[236:237], v[234:235], 0, s[50:51]
	v_cvt_f32_i32_e32 v14, v14
	v_cvt_f32_i32_e32 v15, v15
	v_cvt_f32_i32_e32 v16, v16
	v_cvt_f32_i32_e32 v17, v17
	v_cvt_f32_i32_e32 v10, v10
	v_cvt_f32_i32_e32 v11, v11
	v_cvt_f32_i32_e32 v12, v12
	v_cvt_f32_i32_e32 v13, v13
	v_pk_mul_f32 v[14:15], v[14:15], v[198:199] op_sel_hi:[1,0]
	v_pk_mul_f32 v[16:17], v[16:17], v[198:199] op_sel_hi:[1,0]
	v_pk_mul_f32 v[10:11], v[10:11], v[198:199] op_sel_hi:[1,0]
	v_pk_mul_f32 v[12:13], v[12:13], v[198:199] op_sel_hi:[1,0]
	v_pk_mul_f32 v[14:15], v[14:15], v[216:217]
	v_pk_mul_f32 v[16:17], v[16:17], v[218:219]
	v_pk_mul_f32 v[10:11], v[10:11], v[220:221]
	v_pk_mul_f32 v[12:13], v[12:13], v[222:223]
	v_cvt_pk_bf16_f32 v14, v14, v15
	v_cvt_pk_bf16_f32 v15, v16, v17
	v_cvt_pk_bf16_f32 v16, v10, v11
	v_cvt_pk_bf16_f32 v17, v12, v13
	global_store_dwordx4 v[234:235], v[14:17], off sc1
	v_cvt_f32_i32_e32 v6, v6
	v_cvt_f32_i32_e32 v7, v7
	v_cvt_f32_i32_e32 v8, v8
	v_cvt_f32_i32_e32 v9, v9
	v_cvt_f32_i32_e32 v2, v2
	v_cvt_f32_i32_e32 v3, v3
	v_cvt_f32_i32_e32 v4, v4
	v_cvt_f32_i32_e32 v5, v5
	v_pk_mul_f32 v[6:7], v[6:7], v[198:199] op_sel_hi:[1,0]
	v_pk_mul_f32 v[8:9], v[8:9], v[198:199] op_sel_hi:[1,0]
	v_pk_mul_f32 v[2:3], v[2:3], v[198:199] op_sel_hi:[1,0]
	v_pk_mul_f32 v[4:5], v[4:5], v[198:199] op_sel_hi:[1,0]
	v_pk_mul_f32 v[6:7], v[6:7], v[226:227]
	v_pk_mul_f32 v[8:9], v[8:9], v[228:229]
	v_pk_mul_f32 v[2:3], v[2:3], v[230:231]
	v_pk_mul_f32 v[4:5], v[4:5], v[232:233]
	v_cvt_pk_bf16_f32 v6, v6, v7
	v_cvt_pk_bf16_f32 v7, v8, v9
	v_cvt_pk_bf16_f32 v8, v2, v3
	v_cvt_pk_bf16_f32 v9, v4, v5
	global_store_dwordx4 v[236:237], v[6:9], off sc1
	s_branch .Lfast_tail
.Lfast_silu:
	v_lshl_add_u64 v[236:237], v[234:235], 0, s[50:51]
	v_cvt_f32_i32_e32 v142, v142
	v_cvt_f32_i32_e32 v143, v143
	v_cvt_f32_i32_e32 v144, v144
	v_cvt_f32_i32_e32 v145, v145
	v_cvt_f32_i32_e32 v138, v138
	v_cvt_f32_i32_e32 v139, v139
	v_cvt_f32_i32_e32 v140, v140
	v_cvt_f32_i32_e32 v141, v141
	s_waitcnt lgkmcnt(0)
	v_pk_mul_f32 v[142:143], v[142:143], v[208:209] op_sel_hi:[1,0]
	v_pk_mul_f32 v[144:145], v[144:145], v[208:209] op_sel_hi:[1,0]
	v_pk_mul_f32 v[138:139], v[138:139], v[208:209] op_sel_hi:[1,0]
	v_pk_mul_f32 v[140:141], v[140:141], v[208:209] op_sel_hi:[1,0]
	v_pk_mul_f32 v[142:143], v[142:143], v[216:217]
	v_pk_mul_f32 v[144:145], v[144:145], v[218:219]
	v_pk_mul_f32 v[138:139], v[138:139], v[220:221]
	v_pk_mul_f32 v[140:141], v[140:141], v[222:223]
	v_mul_f32_e32 v240, 0xbfb8aa3b, v142
	v_mul_f32_e32 v241, 0xbfb8aa3b, v143
	v_mul_f32_e32 v242, 0xbfb8aa3b, v144
	v_mul_f32_e32 v243, 0xbfb8aa3b, v145
	v_mul_f32_e32 v244, 0xbfb8aa3b, v138
	v_mul_f32_e32 v245, 0xbfb8aa3b, v139
	v_mul_f32_e32 v246, 0xbfb8aa3b, v140
	v_mul_f32_e32 v247, 0xbfb8aa3b, v141
	v_exp_f32_e32 v240, v240
	v_exp_f32_e32 v241, v241
	v_exp_f32_e32 v242, v242
	v_exp_f32_e32 v243, v243
	v_exp_f32_e32 v244, v244
	v_exp_f32_e32 v245, v245
	v_exp_f32_e32 v246, v246
	v_exp_f32_e32 v247, v247
	v_add_f32_e32 v240, 1.0, v240
	v_add_f32_e32 v241, 1.0, v241
	v_add_f32_e32 v242, 1.0, v242
	v_add_f32_e32 v243, 1.0, v243
	v_add_f32_e32 v244, 1.0, v244
	v_add_f32_e32 v245, 1.0, v245
	v_add_f32_e32 v246, 1.0, v246
	v_add_f32_e32 v247, 1.0, v247
	v_rcp_f32_e32 v240, v240
	v_rcp_f32_e32 v241, v241
	v_rcp_f32_e32 v242, v242
	v_rcp_f32_e32 v243, v243
	v_rcp_f32_e32 v244, v244
	v_rcp_f32_e32 v245, v245
	v_rcp_f32_e32 v246, v246
	v_rcp_f32_e32 v247, v247
	v_pk_mul_f32 v[142:143], v[142:143], v[240:241]
	v_pk_mul_f32 v[144:145], v[144:145], v[242:243]
	v_pk_mul_f32 v[138:139], v[138:139], v[244:245]
	v_pk_mul_f32 v[140:141], v[140:141], v[246:247]
	v_cvt_pk_bf16_f32 v142, v142, v143
	v_cvt_pk_bf16_f32 v143, v144, v145
	v_cvt_pk_bf16_f32 v144, v138, v139
	v_cvt_pk_bf16_f32 v145, v140, v141
	global_store_dwordx4 v[234:235], v[142:145], off sc1
	v_cvt_f32_i32_e32 v134, v134
	v_cvt_f32_i32_e32 v135, v135
	v_cvt_f32_i32_e32 v136, v136
	v_cvt_f32_i32_e32 v137, v137
	v_cvt_f32_i32_e32 v130, v130
	v_cvt_f32_i32_e32 v131, v131
	v_cvt_f32_i32_e32 v132, v132
	v_cvt_f32_i32_e32 v133, v133
	v_pk_mul_f32 v[134:135], v[134:135], v[208:209] op_sel_hi:[1,0]
	v_pk_mul_f32 v[136:137], v[136:137], v[208:209] op_sel_hi:[1,0]
	v_pk_mul_f32 v[130:131], v[130:131], v[208:209] op_sel_hi:[1,0]
	v_pk_mul_f32 v[132:133], v[132:133], v[208:209] op_sel_hi:[1,0]
	v_pk_mul_f32 v[134:135], v[134:135], v[226:227]
	v_pk_mul_f32 v[136:137], v[136:137], v[228:229]
	v_pk_mul_f32 v[130:131], v[130:131], v[230:231]
	v_pk_mul_f32 v[132:133], v[132:133], v[232:233]
	v_mul_f32_e32 v240, 0xbfb8aa3b, v134
	v_mul_f32_e32 v241, 0xbfb8aa3b, v135
	v_mul_f32_e32 v242, 0xbfb8aa3b, v136
	v_mul_f32_e32 v243, 0xbfb8aa3b, v137
	v_mul_f32_e32 v244, 0xbfb8aa3b, v130
	v_mul_f32_e32 v245, 0xbfb8aa3b, v131
	v_mul_f32_e32 v246, 0xbfb8aa3b, v132
	v_mul_f32_e32 v247, 0xbfb8aa3b, v133
	v_exp_f32_e32 v240, v240
	v_exp_f32_e32 v241, v241
	v_exp_f32_e32 v242, v242
	v_exp_f32_e32 v243, v243
	v_exp_f32_e32 v244, v244
	v_exp_f32_e32 v245, v245
	v_exp_f32_e32 v246, v246
	v_exp_f32_e32 v247, v247
	v_add_f32_e32 v240, 1.0, v240
	v_add_f32_e32 v241, 1.0, v241
	v_add_f32_e32 v242, 1.0, v242
	v_add_f32_e32 v243, 1.0, v243
	v_add_f32_e32 v244, 1.0, v244
	v_add_f32_e32 v245, 1.0, v245
	v_add_f32_e32 v246, 1.0, v246
	v_add_f32_e32 v247, 1.0, v247
	v_rcp_f32_e32 v240, v240
	v_rcp_f32_e32 v241, v241
	v_rcp_f32_e32 v242, v242
	v_rcp_f32_e32 v243, v243
	v_rcp_f32_e32 v244, v244
	v_rcp_f32_e32 v245, v245
	v_rcp_f32_e32 v246, v246
	v_rcp_f32_e32 v247, v247
	v_pk_mul_f32 v[134:135], v[134:135], v[240:241]
	v_pk_mul_f32 v[136:137], v[136:137], v[242:243]
	v_pk_mul_f32 v[130:131], v[130:131], v[244:245]
	v_pk_mul_f32 v[132:133], v[132:133], v[246:247]
	v_cvt_pk_bf16_f32 v134, v134, v135
	v_cvt_pk_bf16_f32 v135, v136, v137
	v_cvt_pk_bf16_f32 v136, v130, v131
	v_cvt_pk_bf16_f32 v137, v132, v133
	global_store_dwordx4 v[236:237], v[134:137], off sc1
	v_lshl_add_u64 v[234:235], v[234:235], 0, s[46:47]
	v_lshl_add_u64 v[236:237], v[234:235], 0, s[50:51]
	v_cvt_f32_i32_e32 v126, v126
	v_cvt_f32_i32_e32 v127, v127
	v_cvt_f32_i32_e32 v128, v128
	v_cvt_f32_i32_e32 v129, v129
	v_cvt_f32_i32_e32 v122, v122
	v_cvt_f32_i32_e32 v123, v123
	v_cvt_f32_i32_e32 v124, v124
	v_cvt_f32_i32_e32 v125, v125
	v_pk_mul_f32 v[126:127], v[126:127], v[210:211] op_sel_hi:[1,0]
	v_pk_mul_f32 v[128:129], v[128:129], v[210:211] op_sel_hi:[1,0]
	v_pk_mul_f32 v[122:123], v[122:123], v[210:211] op_sel_hi:[1,0]
	v_pk_mul_f32 v[124:125], v[124:125], v[210:211] op_sel_hi:[1,0]
	v_pk_mul_f32 v[126:127], v[126:127], v[216:217]
	v_pk_mul_f32 v[128:129], v[128:129], v[218:219]
	v_pk_mul_f32 v[122:123], v[122:123], v[220:221]
	v_pk_mul_f32 v[124:125], v[124:125], v[222:223]
	v_mul_f32_e32 v240, 0xbfb8aa3b, v126
	v_mul_f32_e32 v241, 0xbfb8aa3b, v127
	v_mul_f32_e32 v242, 0xbfb8aa3b, v128
	v_mul_f32_e32 v243, 0xbfb8aa3b, v129
	v_mul_f32_e32 v244, 0xbfb8aa3b, v122
	v_mul_f32_e32 v245, 0xbfb8aa3b, v123
	v_mul_f32_e32 v246, 0xbfb8aa3b, v124
	v_mul_f32_e32 v247, 0xbfb8aa3b, v125
	v_exp_f32_e32 v240, v240
	v_exp_f32_e32 v241, v241
	v_exp_f32_e32 v242, v242
	v_exp_f32_e32 v243, v243
	v_exp_f32_e32 v244, v244
	v_exp_f32_e32 v245, v245
	v_exp_f32_e32 v246, v246
	v_exp_f32_e32 v247, v247
	v_add_f32_e32 v240, 1.0, v240
	v_add_f32_e32 v241, 1.0, v241
	v_add_f32_e32 v242, 1.0, v242
	v_add_f32_e32 v243, 1.0, v243
	v_add_f32_e32 v244, 1.0, v244
	v_add_f32_e32 v245, 1.0, v245
	v_add_f32_e32 v246, 1.0, v246
	v_add_f32_e32 v247, 1.0, v247
	v_rcp_f32_e32 v240, v240
	v_rcp_f32_e32 v241, v241
	v_rcp_f32_e32 v242, v242
	v_rcp_f32_e32 v243, v243
	v_rcp_f32_e32 v244, v244
	v_rcp_f32_e32 v245, v245
	v_rcp_f32_e32 v246, v246
	v_rcp_f32_e32 v247, v247
	v_pk_mul_f32 v[126:127], v[126:127], v[240:241]
	v_pk_mul_f32 v[128:129], v[128:129], v[242:243]
	v_pk_mul_f32 v[122:123], v[122:123], v[244:245]
	v_pk_mul_f32 v[124:125], v[124:125], v[246:247]
	v_cvt_pk_bf16_f32 v126, v126, v127
	v_cvt_pk_bf16_f32 v127, v128, v129
	v_cvt_pk_bf16_f32 v128, v122, v123
	v_cvt_pk_bf16_f32 v129, v124, v125
	global_store_dwordx4 v[234:235], v[126:129], off sc1
	v_cvt_f32_i32_e32 v118, v118
	v_cvt_f32_i32_e32 v119, v119
	v_cvt_f32_i32_e32 v120, v120
	v_cvt_f32_i32_e32 v121, v121
	v_cvt_f32_i32_e32 v114, v114
	v_cvt_f32_i32_e32 v115, v115
	v_cvt_f32_i32_e32 v116, v116
	v_cvt_f32_i32_e32 v117, v117
	v_pk_mul_f32 v[118:119], v[118:119], v[210:211] op_sel_hi:[1,0]
	v_pk_mul_f32 v[120:121], v[120:121], v[210:211] op_sel_hi:[1,0]
	v_pk_mul_f32 v[114:115], v[114:115], v[210:211] op_sel_hi:[1,0]
	v_pk_mul_f32 v[116:117], v[116:117], v[210:211] op_sel_hi:[1,0]
	v_pk_mul_f32 v[118:119], v[118:119], v[226:227]
	v_pk_mul_f32 v[120:121], v[120:121], v[228:229]
	v_pk_mul_f32 v[114:115], v[114:115], v[230:231]
	v_pk_mul_f32 v[116:117], v[116:117], v[232:233]
	v_mul_f32_e32 v240, 0xbfb8aa3b, v118
	v_mul_f32_e32 v241, 0xbfb8aa3b, v119
	v_mul_f32_e32 v242, 0xbfb8aa3b, v120
	v_mul_f32_e32 v243, 0xbfb8aa3b, v121
	v_mul_f32_e32 v244, 0xbfb8aa3b, v114
	v_mul_f32_e32 v245, 0xbfb8aa3b, v115
	v_mul_f32_e32 v246, 0xbfb8aa3b, v116
	v_mul_f32_e32 v247, 0xbfb8aa3b, v117
	v_exp_f32_e32 v240, v240
	v_exp_f32_e32 v241, v241
	v_exp_f32_e32 v242, v242
	v_exp_f32_e32 v243, v243
	v_exp_f32_e32 v244, v244
	v_exp_f32_e32 v245, v245
	v_exp_f32_e32 v246, v246
	v_exp_f32_e32 v247, v247
	v_add_f32_e32 v240, 1.0, v240
	v_add_f32_e32 v241, 1.0, v241
	v_add_f32_e32 v242, 1.0, v242
	v_add_f32_e32 v243, 1.0, v243
	v_add_f32_e32 v244, 1.0, v244
	v_add_f32_e32 v245, 1.0, v245
	v_add_f32_e32 v246, 1.0, v246
	v_add_f32_e32 v247, 1.0, v247
	v_rcp_f32_e32 v240, v240
	v_rcp_f32_e32 v241, v241
	v_rcp_f32_e32 v242, v242
	v_rcp_f32_e32 v243, v243
	v_rcp_f32_e32 v244, v244
	v_rcp_f32_e32 v245, v245
	v_rcp_f32_e32 v246, v246
	v_rcp_f32_e32 v247, v247
	v_pk_mul_f32 v[118:119], v[118:119], v[240:241]
	v_pk_mul_f32 v[120:121], v[120:121], v[242:243]
	v_pk_mul_f32 v[114:115], v[114:115], v[244:245]
	v_pk_mul_f32 v[116:117], v[116:117], v[246:247]
	v_cvt_pk_bf16_f32 v118, v118, v119
	v_cvt_pk_bf16_f32 v119, v120, v121
	v_cvt_pk_bf16_f32 v120, v114, v115
	v_cvt_pk_bf16_f32 v121, v116, v117
	global_store_dwordx4 v[236:237], v[118:121], off sc1
	v_lshl_add_u64 v[234:235], v[234:235], 0, s[46:47]
	v_lshl_add_u64 v[236:237], v[234:235], 0, s[50:51]
	v_cvt_f32_i32_e32 v110, v110
	v_cvt_f32_i32_e32 v111, v111
	v_cvt_f32_i32_e32 v112, v112
	v_cvt_f32_i32_e32 v113, v113
	v_cvt_f32_i32_e32 v106, v106
	v_cvt_f32_i32_e32 v107, v107
	v_cvt_f32_i32_e32 v108, v108
	v_cvt_f32_i32_e32 v109, v109
	v_pk_mul_f32 v[110:111], v[110:111], v[212:213] op_sel_hi:[1,0]
	v_pk_mul_f32 v[112:113], v[112:113], v[212:213] op_sel_hi:[1,0]
	v_pk_mul_f32 v[106:107], v[106:107], v[212:213] op_sel_hi:[1,0]
	v_pk_mul_f32 v[108:109], v[108:109], v[212:213] op_sel_hi:[1,0]
	v_pk_mul_f32 v[110:111], v[110:111], v[216:217]
	v_pk_mul_f32 v[112:113], v[112:113], v[218:219]
	v_pk_mul_f32 v[106:107], v[106:107], v[220:221]
	v_pk_mul_f32 v[108:109], v[108:109], v[222:223]
	v_mul_f32_e32 v240, 0xbfb8aa3b, v110
	v_mul_f32_e32 v241, 0xbfb8aa3b, v111
	v_mul_f32_e32 v242, 0xbfb8aa3b, v112
	v_mul_f32_e32 v243, 0xbfb8aa3b, v113
	v_mul_f32_e32 v244, 0xbfb8aa3b, v106
	v_mul_f32_e32 v245, 0xbfb8aa3b, v107
	v_mul_f32_e32 v246, 0xbfb8aa3b, v108
	v_mul_f32_e32 v247, 0xbfb8aa3b, v109
	v_exp_f32_e32 v240, v240
	v_exp_f32_e32 v241, v241
	v_exp_f32_e32 v242, v242
	v_exp_f32_e32 v243, v243
	v_exp_f32_e32 v244, v244
	v_exp_f32_e32 v245, v245
	v_exp_f32_e32 v246, v246
	v_exp_f32_e32 v247, v247
	v_add_f32_e32 v240, 1.0, v240
	v_add_f32_e32 v241, 1.0, v241
	v_add_f32_e32 v242, 1.0, v242
	v_add_f32_e32 v243, 1.0, v243
	v_add_f32_e32 v244, 1.0, v244
	v_add_f32_e32 v245, 1.0, v245
	v_add_f32_e32 v246, 1.0, v246
	v_add_f32_e32 v247, 1.0, v247
	v_rcp_f32_e32 v240, v240
	v_rcp_f32_e32 v241, v241
	v_rcp_f32_e32 v242, v242
	v_rcp_f32_e32 v243, v243
	v_rcp_f32_e32 v244, v244
	v_rcp_f32_e32 v245, v245
	v_rcp_f32_e32 v246, v246
	v_rcp_f32_e32 v247, v247
	v_pk_mul_f32 v[110:111], v[110:111], v[240:241]
	v_pk_mul_f32 v[112:113], v[112:113], v[242:243]
	v_pk_mul_f32 v[106:107], v[106:107], v[244:245]
	v_pk_mul_f32 v[108:109], v[108:109], v[246:247]
	v_cvt_pk_bf16_f32 v110, v110, v111
	v_cvt_pk_bf16_f32 v111, v112, v113
	v_cvt_pk_bf16_f32 v112, v106, v107
	v_cvt_pk_bf16_f32 v113, v108, v109
	global_store_dwordx4 v[234:235], v[110:113], off sc1
	v_cvt_f32_i32_e32 v102, v102
	v_cvt_f32_i32_e32 v103, v103
	v_cvt_f32_i32_e32 v104, v104
	v_cvt_f32_i32_e32 v105, v105
	v_cvt_f32_i32_e32 v98, v98
	v_cvt_f32_i32_e32 v99, v99
	v_cvt_f32_i32_e32 v100, v100
	v_cvt_f32_i32_e32 v101, v101
	v_pk_mul_f32 v[102:103], v[102:103], v[212:213] op_sel_hi:[1,0]
	v_pk_mul_f32 v[104:105], v[104:105], v[212:213] op_sel_hi:[1,0]
	v_pk_mul_f32 v[98:99], v[98:99], v[212:213] op_sel_hi:[1,0]
	v_pk_mul_f32 v[100:101], v[100:101], v[212:213] op_sel_hi:[1,0]
	v_pk_mul_f32 v[102:103], v[102:103], v[226:227]
	v_pk_mul_f32 v[104:105], v[104:105], v[228:229]
	v_pk_mul_f32 v[98:99], v[98:99], v[230:231]
	v_pk_mul_f32 v[100:101], v[100:101], v[232:233]
	v_mul_f32_e32 v240, 0xbfb8aa3b, v102
	v_mul_f32_e32 v241, 0xbfb8aa3b, v103
	v_mul_f32_e32 v242, 0xbfb8aa3b, v104
	v_mul_f32_e32 v243, 0xbfb8aa3b, v105
	v_mul_f32_e32 v244, 0xbfb8aa3b, v98
	v_mul_f32_e32 v245, 0xbfb8aa3b, v99
	v_mul_f32_e32 v246, 0xbfb8aa3b, v100
	v_mul_f32_e32 v247, 0xbfb8aa3b, v101
	v_exp_f32_e32 v240, v240
	v_exp_f32_e32 v241, v241
	v_exp_f32_e32 v242, v242
	v_exp_f32_e32 v243, v243
	v_exp_f32_e32 v244, v244
	v_exp_f32_e32 v245, v245
	v_exp_f32_e32 v246, v246
	v_exp_f32_e32 v247, v247
	v_add_f32_e32 v240, 1.0, v240
	v_add_f32_e32 v241, 1.0, v241
	v_add_f32_e32 v242, 1.0, v242
	v_add_f32_e32 v243, 1.0, v243
	v_add_f32_e32 v244, 1.0, v244
	v_add_f32_e32 v245, 1.0, v245
	v_add_f32_e32 v246, 1.0, v246
	v_add_f32_e32 v247, 1.0, v247
	v_rcp_f32_e32 v240, v240
	v_rcp_f32_e32 v241, v241
	v_rcp_f32_e32 v242, v242
	v_rcp_f32_e32 v243, v243
	v_rcp_f32_e32 v244, v244
	v_rcp_f32_e32 v245, v245
	v_rcp_f32_e32 v246, v246
	v_rcp_f32_e32 v247, v247
	v_pk_mul_f32 v[102:103], v[102:103], v[240:241]
	v_pk_mul_f32 v[104:105], v[104:105], v[242:243]
	v_pk_mul_f32 v[98:99], v[98:99], v[244:245]
	v_pk_mul_f32 v[100:101], v[100:101], v[246:247]
	v_cvt_pk_bf16_f32 v102, v102, v103
	v_cvt_pk_bf16_f32 v103, v104, v105
	v_cvt_pk_bf16_f32 v104, v98, v99
	v_cvt_pk_bf16_f32 v105, v100, v101
	global_store_dwordx4 v[236:237], v[102:105], off sc1
	v_lshl_add_u64 v[234:235], v[234:235], 0, s[46:47]
	v_lshl_add_u64 v[236:237], v[234:235], 0, s[50:51]
	v_cvt_f32_i32_e32 v94, v94
	v_cvt_f32_i32_e32 v95, v95
	v_cvt_f32_i32_e32 v96, v96
	v_cvt_f32_i32_e32 v97, v97
	v_cvt_f32_i32_e32 v90, v90
	v_cvt_f32_i32_e32 v91, v91
	v_cvt_f32_i32_e32 v92, v92
	v_cvt_f32_i32_e32 v93, v93
	v_pk_mul_f32 v[94:95], v[94:95], v[214:215] op_sel_hi:[1,0]
	v_pk_mul_f32 v[96:97], v[96:97], v[214:215] op_sel_hi:[1,0]
	v_pk_mul_f32 v[90:91], v[90:91], v[214:215] op_sel_hi:[1,0]
	v_pk_mul_f32 v[92:93], v[92:93], v[214:215] op_sel_hi:[1,0]
	v_pk_mul_f32 v[94:95], v[94:95], v[216:217]
	v_pk_mul_f32 v[96:97], v[96:97], v[218:219]
	v_pk_mul_f32 v[90:91], v[90:91], v[220:221]
	v_pk_mul_f32 v[92:93], v[92:93], v[222:223]
	v_mul_f32_e32 v240, 0xbfb8aa3b, v94
	v_mul_f32_e32 v241, 0xbfb8aa3b, v95
	v_mul_f32_e32 v242, 0xbfb8aa3b, v96
	v_mul_f32_e32 v243, 0xbfb8aa3b, v97
	v_mul_f32_e32 v244, 0xbfb8aa3b, v90
	v_mul_f32_e32 v245, 0xbfb8aa3b, v91
	v_mul_f32_e32 v246, 0xbfb8aa3b, v92
	v_mul_f32_e32 v247, 0xbfb8aa3b, v93
	v_exp_f32_e32 v240, v240
	v_exp_f32_e32 v241, v241
	v_exp_f32_e32 v242, v242
	v_exp_f32_e32 v243, v243
	v_exp_f32_e32 v244, v244
	v_exp_f32_e32 v245, v245
	v_exp_f32_e32 v246, v246
	v_exp_f32_e32 v247, v247
	v_add_f32_e32 v240, 1.0, v240
	v_add_f32_e32 v241, 1.0, v241
	v_add_f32_e32 v242, 1.0, v242
	v_add_f32_e32 v243, 1.0, v243
	v_add_f32_e32 v244, 1.0, v244
	v_add_f32_e32 v245, 1.0, v245
	v_add_f32_e32 v246, 1.0, v246
	v_add_f32_e32 v247, 1.0, v247
	v_rcp_f32_e32 v240, v240
	v_rcp_f32_e32 v241, v241
	v_rcp_f32_e32 v242, v242
	v_rcp_f32_e32 v243, v243
	v_rcp_f32_e32 v244, v244
	v_rcp_f32_e32 v245, v245
	v_rcp_f32_e32 v246, v246
	v_rcp_f32_e32 v247, v247
	v_pk_mul_f32 v[94:95], v[94:95], v[240:241]
	v_pk_mul_f32 v[96:97], v[96:97], v[242:243]
	v_pk_mul_f32 v[90:91], v[90:91], v[244:245]
	v_pk_mul_f32 v[92:93], v[92:93], v[246:247]
	v_cvt_pk_bf16_f32 v94, v94, v95
	v_cvt_pk_bf16_f32 v95, v96, v97
	v_cvt_pk_bf16_f32 v96, v90, v91
	v_cvt_pk_bf16_f32 v97, v92, v93
	global_store_dwordx4 v[234:235], v[94:97], off sc1
	v_cvt_f32_i32_e32 v86, v86
	v_cvt_f32_i32_e32 v87, v87
	v_cvt_f32_i32_e32 v88, v88
	v_cvt_f32_i32_e32 v89, v89
	v_cvt_f32_i32_e32 v82, v82
	v_cvt_f32_i32_e32 v83, v83
	v_cvt_f32_i32_e32 v84, v84
	v_cvt_f32_i32_e32 v85, v85
	v_pk_mul_f32 v[86:87], v[86:87], v[214:215] op_sel_hi:[1,0]
	v_pk_mul_f32 v[88:89], v[88:89], v[214:215] op_sel_hi:[1,0]
	v_pk_mul_f32 v[82:83], v[82:83], v[214:215] op_sel_hi:[1,0]
	v_pk_mul_f32 v[84:85], v[84:85], v[214:215] op_sel_hi:[1,0]
	v_pk_mul_f32 v[86:87], v[86:87], v[226:227]
	v_pk_mul_f32 v[88:89], v[88:89], v[228:229]
	v_pk_mul_f32 v[82:83], v[82:83], v[230:231]
	v_pk_mul_f32 v[84:85], v[84:85], v[232:233]
	v_mul_f32_e32 v240, 0xbfb8aa3b, v86
	v_mul_f32_e32 v241, 0xbfb8aa3b, v87
	v_mul_f32_e32 v242, 0xbfb8aa3b, v88
	v_mul_f32_e32 v243, 0xbfb8aa3b, v89
	v_mul_f32_e32 v244, 0xbfb8aa3b, v82
	v_mul_f32_e32 v245, 0xbfb8aa3b, v83
	v_mul_f32_e32 v246, 0xbfb8aa3b, v84
	v_mul_f32_e32 v247, 0xbfb8aa3b, v85
	v_exp_f32_e32 v240, v240
	v_exp_f32_e32 v241, v241
	v_exp_f32_e32 v242, v242
	v_exp_f32_e32 v243, v243
	v_exp_f32_e32 v244, v244
	v_exp_f32_e32 v245, v245
	v_exp_f32_e32 v246, v246
	v_exp_f32_e32 v247, v247
	v_add_f32_e32 v240, 1.0, v240
	v_add_f32_e32 v241, 1.0, v241
	v_add_f32_e32 v242, 1.0, v242
	v_add_f32_e32 v243, 1.0, v243
	v_add_f32_e32 v244, 1.0, v244
	v_add_f32_e32 v245, 1.0, v245
	v_add_f32_e32 v246, 1.0, v246
	v_add_f32_e32 v247, 1.0, v247
	v_rcp_f32_e32 v240, v240
	v_rcp_f32_e32 v241, v241
	v_rcp_f32_e32 v242, v242
	v_rcp_f32_e32 v243, v243
	v_rcp_f32_e32 v244, v244
	v_rcp_f32_e32 v245, v245
	v_rcp_f32_e32 v246, v246
	v_rcp_f32_e32 v247, v247
	v_pk_mul_f32 v[86:87], v[86:87], v[240:241]
	v_pk_mul_f32 v[88:89], v[88:89], v[242:243]
	v_pk_mul_f32 v[82:83], v[82:83], v[244:245]
	v_pk_mul_f32 v[84:85], v[84:85], v[246:247]
	v_cvt_pk_bf16_f32 v86, v86, v87
	v_cvt_pk_bf16_f32 v87, v88, v89
	v_cvt_pk_bf16_f32 v88, v82, v83
	v_cvt_pk_bf16_f32 v89, v84, v85
	global_store_dwordx4 v[236:237], v[86:89], off sc1
	v_lshl_add_u64 v[234:235], v[234:235], 0, s[48:49]
	v_lshl_add_u64 v[236:237], v[234:235], 0, s[50:51]
	v_cvt_f32_i32_e32 v78, v78
	v_cvt_f32_i32_e32 v79, v79
	v_cvt_f32_i32_e32 v80, v80
	v_cvt_f32_i32_e32 v81, v81
	v_cvt_f32_i32_e32 v74, v74
	v_cvt_f32_i32_e32 v75, v75
	v_cvt_f32_i32_e32 v76, v76
	v_cvt_f32_i32_e32 v77, v77
	v_pk_mul_f32 v[78:79], v[78:79], v[178:179] op_sel_hi:[1,0]
	v_pk_mul_f32 v[80:81], v[80:81], v[178:179] op_sel_hi:[1,0]
	v_pk_mul_f32 v[74:75], v[74:75], v[178:179] op_sel_hi:[1,0]
	v_pk_mul_f32 v[76:77], v[76:77], v[178:179] op_sel_hi:[1,0]
	v_pk_mul_f32 v[78:79], v[78:79], v[216:217]
	v_pk_mul_f32 v[80:81], v[80:81], v[218:219]
	v_pk_mul_f32 v[74:75], v[74:75], v[220:221]
	v_pk_mul_f32 v[76:77], v[76:77], v[222:223]
	v_mul_f32_e32 v240, 0xbfb8aa3b, v78
	v_mul_f32_e32 v241, 0xbfb8aa3b, v79
	v_mul_f32_e32 v242, 0xbfb8aa3b, v80
	v_mul_f32_e32 v243, 0xbfb8aa3b, v81
	v_mul_f32_e32 v244, 0xbfb8aa3b, v74
	v_mul_f32_e32 v245, 0xbfb8aa3b, v75
	v_mul_f32_e32 v246, 0xbfb8aa3b, v76
	v_mul_f32_e32 v247, 0xbfb8aa3b, v77
	v_exp_f32_e32 v240, v240
	v_exp_f32_e32 v241, v241
	v_exp_f32_e32 v242, v242
	v_exp_f32_e32 v243, v243
	v_exp_f32_e32 v244, v244
	v_exp_f32_e32 v245, v245
	v_exp_f32_e32 v246, v246
	v_exp_f32_e32 v247, v247
	v_add_f32_e32 v240, 1.0, v240
	v_add_f32_e32 v241, 1.0, v241
	v_add_f32_e32 v242, 1.0, v242
	v_add_f32_e32 v243, 1.0, v243
	v_add_f32_e32 v244, 1.0, v244
	v_add_f32_e32 v245, 1.0, v245
	v_add_f32_e32 v246, 1.0, v246
	v_add_f32_e32 v247, 1.0, v247
	v_rcp_f32_e32 v240, v240
	v_rcp_f32_e32 v241, v241
	v_rcp_f32_e32 v242, v242
	v_rcp_f32_e32 v243, v243
	v_rcp_f32_e32 v244, v244
	v_rcp_f32_e32 v245, v245
	v_rcp_f32_e32 v246, v246
	v_rcp_f32_e32 v247, v247
	v_pk_mul_f32 v[78:79], v[78:79], v[240:241]
	v_pk_mul_f32 v[80:81], v[80:81], v[242:243]
	v_pk_mul_f32 v[74:75], v[74:75], v[244:245]
	v_pk_mul_f32 v[76:77], v[76:77], v[246:247]
	v_cvt_pk_bf16_f32 v78, v78, v79
	v_cvt_pk_bf16_f32 v79, v80, v81
	v_cvt_pk_bf16_f32 v80, v74, v75
	v_cvt_pk_bf16_f32 v81, v76, v77
	global_store_dwordx4 v[234:235], v[78:81], off sc1
	v_cvt_f32_i32_e32 v70, v70
	v_cvt_f32_i32_e32 v71, v71
	v_cvt_f32_i32_e32 v72, v72
	v_cvt_f32_i32_e32 v73, v73
	v_cvt_f32_i32_e32 v66, v66
	v_cvt_f32_i32_e32 v67, v67
	v_cvt_f32_i32_e32 v68, v68
	v_cvt_f32_i32_e32 v69, v69
	v_pk_mul_f32 v[70:71], v[70:71], v[178:179] op_sel_hi:[1,0]
	v_pk_mul_f32 v[72:73], v[72:73], v[178:179] op_sel_hi:[1,0]
	v_pk_mul_f32 v[66:67], v[66:67], v[178:179] op_sel_hi:[1,0]
	v_pk_mul_f32 v[68:69], v[68:69], v[178:179] op_sel_hi:[1,0]
	v_pk_mul_f32 v[70:71], v[70:71], v[226:227]
	v_pk_mul_f32 v[72:73], v[72:73], v[228:229]
	v_pk_mul_f32 v[66:67], v[66:67], v[230:231]
	v_pk_mul_f32 v[68:69], v[68:69], v[232:233]
	v_mul_f32_e32 v240, 0xbfb8aa3b, v70
	v_mul_f32_e32 v241, 0xbfb8aa3b, v71
	v_mul_f32_e32 v242, 0xbfb8aa3b, v72
	v_mul_f32_e32 v243, 0xbfb8aa3b, v73
	v_mul_f32_e32 v244, 0xbfb8aa3b, v66
	v_mul_f32_e32 v245, 0xbfb8aa3b, v67
	v_mul_f32_e32 v246, 0xbfb8aa3b, v68
	v_mul_f32_e32 v247, 0xbfb8aa3b, v69
	v_exp_f32_e32 v240, v240
	v_exp_f32_e32 v241, v241
	v_exp_f32_e32 v242, v242
	v_exp_f32_e32 v243, v243
	v_exp_f32_e32 v244, v244
	v_exp_f32_e32 v245, v245
	v_exp_f32_e32 v246, v246
	v_exp_f32_e32 v247, v247
	v_add_f32_e32 v240, 1.0, v240
	v_add_f32_e32 v241, 1.0, v241
	v_add_f32_e32 v242, 1.0, v242
	v_add_f32_e32 v243, 1.0, v243
	v_add_f32_e32 v244, 1.0, v244
	v_add_f32_e32 v245, 1.0, v245
	v_add_f32_e32 v246, 1.0, v246
	v_add_f32_e32 v247, 1.0, v247
	v_rcp_f32_e32 v240, v240
	v_rcp_f32_e32 v241, v241
	v_rcp_f32_e32 v242, v242
	v_rcp_f32_e32 v243, v243
	v_rcp_f32_e32 v244, v244
	v_rcp_f32_e32 v245, v245
	v_rcp_f32_e32 v246, v246
	v_rcp_f32_e32 v247, v247
	v_pk_mul_f32 v[70:71], v[70:71], v[240:241]
	v_pk_mul_f32 v[72:73], v[72:73], v[242:243]
	v_pk_mul_f32 v[66:67], v[66:67], v[244:245]
	v_pk_mul_f32 v[68:69], v[68:69], v[246:247]
	v_cvt_pk_bf16_f32 v70, v70, v71
	v_cvt_pk_bf16_f32 v71, v72, v73
	v_cvt_pk_bf16_f32 v72, v66, v67
	v_cvt_pk_bf16_f32 v73, v68, v69
	global_store_dwordx4 v[236:237], v[70:73], off sc1
	v_lshl_add_u64 v[234:235], v[234:235], 0, s[46:47]
	v_lshl_add_u64 v[236:237], v[234:235], 0, s[50:51]
	v_cvt_f32_i32_e32 v62, v62
	v_cvt_f32_i32_e32 v63, v63
	v_cvt_f32_i32_e32 v64, v64
	v_cvt_f32_i32_e32 v65, v65
	v_cvt_f32_i32_e32 v58, v58
	v_cvt_f32_i32_e32 v59, v59
	v_cvt_f32_i32_e32 v60, v60
	v_cvt_f32_i32_e32 v61, v61
	v_pk_mul_f32 v[62:63], v[62:63], v[180:181] op_sel_hi:[1,0]
	v_pk_mul_f32 v[64:65], v[64:65], v[180:181] op_sel_hi:[1,0]
	v_pk_mul_f32 v[58:59], v[58:59], v[180:181] op_sel_hi:[1,0]
	v_pk_mul_f32 v[60:61], v[60:61], v[180:181] op_sel_hi:[1,0]
	v_pk_mul_f32 v[62:63], v[62:63], v[216:217]
	v_pk_mul_f32 v[64:65], v[64:65], v[218:219]
	v_pk_mul_f32 v[58:59], v[58:59], v[220:221]
	v_pk_mul_f32 v[60:61], v[60:61], v[222:223]
	v_mul_f32_e32 v240, 0xbfb8aa3b, v62
	v_mul_f32_e32 v241, 0xbfb8aa3b, v63
	v_mul_f32_e32 v242, 0xbfb8aa3b, v64
	v_mul_f32_e32 v243, 0xbfb8aa3b, v65
	v_mul_f32_e32 v244, 0xbfb8aa3b, v58
	v_mul_f32_e32 v245, 0xbfb8aa3b, v59
	v_mul_f32_e32 v246, 0xbfb8aa3b, v60
	v_mul_f32_e32 v247, 0xbfb8aa3b, v61
	v_exp_f32_e32 v240, v240
	v_exp_f32_e32 v241, v241
	v_exp_f32_e32 v242, v242
	v_exp_f32_e32 v243, v243
	v_exp_f32_e32 v244, v244
	v_exp_f32_e32 v245, v245
	v_exp_f32_e32 v246, v246
	v_exp_f32_e32 v247, v247
	v_add_f32_e32 v240, 1.0, v240
	v_add_f32_e32 v241, 1.0, v241
	v_add_f32_e32 v242, 1.0, v242
	v_add_f32_e32 v243, 1.0, v243
	v_add_f32_e32 v244, 1.0, v244
	v_add_f32_e32 v245, 1.0, v245
	v_add_f32_e32 v246, 1.0, v246
	v_add_f32_e32 v247, 1.0, v247
	v_rcp_f32_e32 v240, v240
	v_rcp_f32_e32 v241, v241
	v_rcp_f32_e32 v242, v242
	v_rcp_f32_e32 v243, v243
	v_rcp_f32_e32 v244, v244
	v_rcp_f32_e32 v245, v245
	v_rcp_f32_e32 v246, v246
	v_rcp_f32_e32 v247, v247
	v_pk_mul_f32 v[62:63], v[62:63], v[240:241]
	v_pk_mul_f32 v[64:65], v[64:65], v[242:243]
	v_pk_mul_f32 v[58:59], v[58:59], v[244:245]
	v_pk_mul_f32 v[60:61], v[60:61], v[246:247]
	v_cvt_pk_bf16_f32 v62, v62, v63
	v_cvt_pk_bf16_f32 v63, v64, v65
	v_cvt_pk_bf16_f32 v64, v58, v59
	v_cvt_pk_bf16_f32 v65, v60, v61
	global_store_dwordx4 v[234:235], v[62:65], off sc1
	v_cvt_f32_i32_e32 v54, v54
	v_cvt_f32_i32_e32 v55, v55
	v_cvt_f32_i32_e32 v56, v56
	v_cvt_f32_i32_e32 v57, v57
	v_cvt_f32_i32_e32 v50, v50
	v_cvt_f32_i32_e32 v51, v51
	v_cvt_f32_i32_e32 v52, v52
	v_cvt_f32_i32_e32 v53, v53
	v_pk_mul_f32 v[54:55], v[54:55], v[180:181] op_sel_hi:[1,0]
	v_pk_mul_f32 v[56:57], v[56:57], v[180:181] op_sel_hi:[1,0]
	v_pk_mul_f32 v[50:51], v[50:51], v[180:181] op_sel_hi:[1,0]
	v_pk_mul_f32 v[52:53], v[52:53], v[180:181] op_sel_hi:[1,0]
	v_pk_mul_f32 v[54:55], v[54:55], v[226:227]
	v_pk_mul_f32 v[56:57], v[56:57], v[228:229]
	v_pk_mul_f32 v[50:51], v[50:51], v[230:231]
	v_pk_mul_f32 v[52:53], v[52:53], v[232:233]
	v_mul_f32_e32 v240, 0xbfb8aa3b, v54
	v_mul_f32_e32 v241, 0xbfb8aa3b, v55
	v_mul_f32_e32 v242, 0xbfb8aa3b, v56
	v_mul_f32_e32 v243, 0xbfb8aa3b, v57
	v_mul_f32_e32 v244, 0xbfb8aa3b, v50
	v_mul_f32_e32 v245, 0xbfb8aa3b, v51
	v_mul_f32_e32 v246, 0xbfb8aa3b, v52
	v_mul_f32_e32 v247, 0xbfb8aa3b, v53
	v_exp_f32_e32 v240, v240
	v_exp_f32_e32 v241, v241
	v_exp_f32_e32 v242, v242
	v_exp_f32_e32 v243, v243
	v_exp_f32_e32 v244, v244
	v_exp_f32_e32 v245, v245
	v_exp_f32_e32 v246, v246
	v_exp_f32_e32 v247, v247
	v_add_f32_e32 v240, 1.0, v240
	v_add_f32_e32 v241, 1.0, v241
	v_add_f32_e32 v242, 1.0, v242
	v_add_f32_e32 v243, 1.0, v243
	v_add_f32_e32 v244, 1.0, v244
	v_add_f32_e32 v245, 1.0, v245
	v_add_f32_e32 v246, 1.0, v246
	v_add_f32_e32 v247, 1.0, v247
	v_rcp_f32_e32 v240, v240
	v_rcp_f32_e32 v241, v241
	v_rcp_f32_e32 v242, v242
	v_rcp_f32_e32 v243, v243
	v_rcp_f32_e32 v244, v244
	v_rcp_f32_e32 v245, v245
	v_rcp_f32_e32 v246, v246
	v_rcp_f32_e32 v247, v247
	v_pk_mul_f32 v[54:55], v[54:55], v[240:241]
	v_pk_mul_f32 v[56:57], v[56:57], v[242:243]
	v_pk_mul_f32 v[50:51], v[50:51], v[244:245]
	v_pk_mul_f32 v[52:53], v[52:53], v[246:247]
	v_cvt_pk_bf16_f32 v54, v54, v55
	v_cvt_pk_bf16_f32 v55, v56, v57
	v_cvt_pk_bf16_f32 v56, v50, v51
	v_cvt_pk_bf16_f32 v57, v52, v53
	global_store_dwordx4 v[236:237], v[54:57], off sc1
	v_lshl_add_u64 v[234:235], v[234:235], 0, s[46:47]
	v_lshl_add_u64 v[236:237], v[234:235], 0, s[50:51]
	v_cvt_f32_i32_e32 v46, v46
	v_cvt_f32_i32_e32 v47, v47
	v_cvt_f32_i32_e32 v48, v48
	v_cvt_f32_i32_e32 v49, v49
	v_cvt_f32_i32_e32 v42, v42
	v_cvt_f32_i32_e32 v43, v43
	v_cvt_f32_i32_e32 v44, v44
	v_cvt_f32_i32_e32 v45, v45
	v_pk_mul_f32 v[46:47], v[46:47], v[196:197] op_sel_hi:[1,0]
	v_pk_mul_f32 v[48:49], v[48:49], v[196:197] op_sel_hi:[1,0]
	v_pk_mul_f32 v[42:43], v[42:43], v[196:197] op_sel_hi:[1,0]
	v_pk_mul_f32 v[44:45], v[44:45], v[196:197] op_sel_hi:[1,0]
	v_pk_mul_f32 v[46:47], v[46:47], v[216:217]
	v_pk_mul_f32 v[48:49], v[48:49], v[218:219]
	v_pk_mul_f32 v[42:43], v[42:43], v[220:221]
	v_pk_mul_f32 v[44:45], v[44:45], v[222:223]
	v_mul_f32_e32 v240, 0xbfb8aa3b, v46
	v_mul_f32_e32 v241, 0xbfb8aa3b, v47
	v_mul_f32_e32 v242, 0xbfb8aa3b, v48
	v_mul_f32_e32 v243, 0xbfb8aa3b, v49
	v_mul_f32_e32 v244, 0xbfb8aa3b, v42
	v_mul_f32_e32 v245, 0xbfb8aa3b, v43
	v_mul_f32_e32 v246, 0xbfb8aa3b, v44
	v_mul_f32_e32 v247, 0xbfb8aa3b, v45
	v_exp_f32_e32 v240, v240
	v_exp_f32_e32 v241, v241
	v_exp_f32_e32 v242, v242
	v_exp_f32_e32 v243, v243
	v_exp_f32_e32 v244, v244
	v_exp_f32_e32 v245, v245
	v_exp_f32_e32 v246, v246
	v_exp_f32_e32 v247, v247
	v_add_f32_e32 v240, 1.0, v240
	v_add_f32_e32 v241, 1.0, v241
	v_add_f32_e32 v242, 1.0, v242
	v_add_f32_e32 v243, 1.0, v243
	v_add_f32_e32 v244, 1.0, v244
	v_add_f32_e32 v245, 1.0, v245
	v_add_f32_e32 v246, 1.0, v246
	v_add_f32_e32 v247, 1.0, v247
	v_rcp_f32_e32 v240, v240
	v_rcp_f32_e32 v241, v241
	v_rcp_f32_e32 v242, v242
	v_rcp_f32_e32 v243, v243
	v_rcp_f32_e32 v244, v244
	v_rcp_f32_e32 v245, v245
	v_rcp_f32_e32 v246, v246
	v_rcp_f32_e32 v247, v247
	v_pk_mul_f32 v[46:47], v[46:47], v[240:241]
	v_pk_mul_f32 v[48:49], v[48:49], v[242:243]
	v_pk_mul_f32 v[42:43], v[42:43], v[244:245]
	v_pk_mul_f32 v[44:45], v[44:45], v[246:247]
	v_cvt_pk_bf16_f32 v46, v46, v47
	v_cvt_pk_bf16_f32 v47, v48, v49
	v_cvt_pk_bf16_f32 v48, v42, v43
	v_cvt_pk_bf16_f32 v49, v44, v45
	global_store_dwordx4 v[234:235], v[46:49], off sc1
	v_cvt_f32_i32_e32 v30, v30
	v_cvt_f32_i32_e32 v31, v31
	v_cvt_f32_i32_e32 v32, v32
	v_cvt_f32_i32_e32 v33, v33
	v_cvt_f32_i32_e32 v26, v26
	v_cvt_f32_i32_e32 v27, v27
	v_cvt_f32_i32_e32 v28, v28
	v_cvt_f32_i32_e32 v29, v29
	v_pk_mul_f32 v[30:31], v[30:31], v[196:197] op_sel_hi:[1,0]
	v_pk_mul_f32 v[32:33], v[32:33], v[196:197] op_sel_hi:[1,0]
	v_pk_mul_f32 v[26:27], v[26:27], v[196:197] op_sel_hi:[1,0]
	v_pk_mul_f32 v[28:29], v[28:29], v[196:197] op_sel_hi:[1,0]
	v_pk_mul_f32 v[30:31], v[30:31], v[226:227]
	v_pk_mul_f32 v[32:33], v[32:33], v[228:229]
	v_pk_mul_f32 v[26:27], v[26:27], v[230:231]
	v_pk_mul_f32 v[28:29], v[28:29], v[232:233]
	v_mul_f32_e32 v240, 0xbfb8aa3b, v30
	v_mul_f32_e32 v241, 0xbfb8aa3b, v31
	v_mul_f32_e32 v242, 0xbfb8aa3b, v32
	v_mul_f32_e32 v243, 0xbfb8aa3b, v33
	v_mul_f32_e32 v244, 0xbfb8aa3b, v26
	v_mul_f32_e32 v245, 0xbfb8aa3b, v27
	v_mul_f32_e32 v246, 0xbfb8aa3b, v28
	v_mul_f32_e32 v247, 0xbfb8aa3b, v29
	v_exp_f32_e32 v240, v240
	v_exp_f32_e32 v241, v241
	v_exp_f32_e32 v242, v242
	v_exp_f32_e32 v243, v243
	v_exp_f32_e32 v244, v244
	v_exp_f32_e32 v245, v245
	v_exp_f32_e32 v246, v246
	v_exp_f32_e32 v247, v247
	v_add_f32_e32 v240, 1.0, v240
	v_add_f32_e32 v241, 1.0, v241
	v_add_f32_e32 v242, 1.0, v242
	v_add_f32_e32 v243, 1.0, v243
	v_add_f32_e32 v244, 1.0, v244
	v_add_f32_e32 v245, 1.0, v245
	v_add_f32_e32 v246, 1.0, v246
	v_add_f32_e32 v247, 1.0, v247
	v_rcp_f32_e32 v240, v240
	v_rcp_f32_e32 v241, v241
	v_rcp_f32_e32 v242, v242
	v_rcp_f32_e32 v243, v243
	v_rcp_f32_e32 v244, v244
	v_rcp_f32_e32 v245, v245
	v_rcp_f32_e32 v246, v246
	v_rcp_f32_e32 v247, v247
	v_pk_mul_f32 v[30:31], v[30:31], v[240:241]
	v_pk_mul_f32 v[32:33], v[32:33], v[242:243]
	v_pk_mul_f32 v[26:27], v[26:27], v[244:245]
	v_pk_mul_f32 v[28:29], v[28:29], v[246:247]
	v_cvt_pk_bf16_f32 v30, v30, v31
	v_cvt_pk_bf16_f32 v31, v32, v33
	v_cvt_pk_bf16_f32 v32, v26, v27
	v_cvt_pk_bf16_f32 v33, v28, v29
	global_store_dwordx4 v[236:237], v[30:33], off sc1
	v_lshl_add_u64 v[234:235], v[234:235], 0, s[46:47]
	v_lshl_add_u64 v[236:237], v[234:235], 0, s[50:51]
	v_cvt_f32_i32_e32 v14, v14
	v_cvt_f32_i32_e32 v15, v15
	v_cvt_f32_i32_e32 v16, v16
	v_cvt_f32_i32_e32 v17, v17
	v_cvt_f32_i32_e32 v10, v10
	v_cvt_f32_i32_e32 v11, v11
	v_cvt_f32_i32_e32 v12, v12
	v_cvt_f32_i32_e32 v13, v13
	v_pk_mul_f32 v[14:15], v[14:15], v[198:199] op_sel_hi:[1,0]
	v_pk_mul_f32 v[16:17], v[16:17], v[198:199] op_sel_hi:[1,0]
	v_pk_mul_f32 v[10:11], v[10:11], v[198:199] op_sel_hi:[1,0]
	v_pk_mul_f32 v[12:13], v[12:13], v[198:199] op_sel_hi:[1,0]
	v_pk_mul_f32 v[14:15], v[14:15], v[216:217]
	v_pk_mul_f32 v[16:17], v[16:17], v[218:219]
	v_pk_mul_f32 v[10:11], v[10:11], v[220:221]
	v_pk_mul_f32 v[12:13], v[12:13], v[222:223]
	v_mul_f32_e32 v240, 0xbfb8aa3b, v14
	v_mul_f32_e32 v241, 0xbfb8aa3b, v15
	v_mul_f32_e32 v242, 0xbfb8aa3b, v16
	v_mul_f32_e32 v243, 0xbfb8aa3b, v17
	v_mul_f32_e32 v244, 0xbfb8aa3b, v10
	v_mul_f32_e32 v245, 0xbfb8aa3b, v11
	v_mul_f32_e32 v246, 0xbfb8aa3b, v12
	v_mul_f32_e32 v247, 0xbfb8aa3b, v13
	v_exp_f32_e32 v240, v240
	v_exp_f32_e32 v241, v241
	v_exp_f32_e32 v242, v242
	v_exp_f32_e32 v243, v243
	v_exp_f32_e32 v244, v244
	v_exp_f32_e32 v245, v245
	v_exp_f32_e32 v246, v246
	v_exp_f32_e32 v247, v247
	v_add_f32_e32 v240, 1.0, v240
	v_add_f32_e32 v241, 1.0, v241
	v_add_f32_e32 v242, 1.0, v242
	v_add_f32_e32 v243, 1.0, v243
	v_add_f32_e32 v244, 1.0, v244
	v_add_f32_e32 v245, 1.0, v245
	v_add_f32_e32 v246, 1.0, v246
	v_add_f32_e32 v247, 1.0, v247
	v_rcp_f32_e32 v240, v240
	v_rcp_f32_e32 v241, v241
	v_rcp_f32_e32 v242, v242
	v_rcp_f32_e32 v243, v243
	v_rcp_f32_e32 v244, v244
	v_rcp_f32_e32 v245, v245
	v_rcp_f32_e32 v246, v246
	v_rcp_f32_e32 v247, v247
	v_pk_mul_f32 v[14:15], v[14:15], v[240:241]
	v_pk_mul_f32 v[16:17], v[16:17], v[242:243]
	v_pk_mul_f32 v[10:11], v[10:11], v[244:245]
	v_pk_mul_f32 v[12:13], v[12:13], v[246:247]
	v_cvt_pk_bf16_f32 v14, v14, v15
	v_cvt_pk_bf16_f32 v15, v16, v17
	v_cvt_pk_bf16_f32 v16, v10, v11
	v_cvt_pk_bf16_f32 v17, v12, v13
	global_store_dwordx4 v[234:235], v[14:17], off sc1
	v_cvt_f32_i32_e32 v6, v6
	v_cvt_f32_i32_e32 v7, v7
	v_cvt_f32_i32_e32 v8, v8
	v_cvt_f32_i32_e32 v9, v9
	v_cvt_f32_i32_e32 v2, v2
	v_cvt_f32_i32_e32 v3, v3
	v_cvt_f32_i32_e32 v4, v4
	v_cvt_f32_i32_e32 v5, v5
	v_pk_mul_f32 v[6:7], v[6:7], v[198:199] op_sel_hi:[1,0]
	v_pk_mul_f32 v[8:9], v[8:9], v[198:199] op_sel_hi:[1,0]
	v_pk_mul_f32 v[2:3], v[2:3], v[198:199] op_sel_hi:[1,0]
	v_pk_mul_f32 v[4:5], v[4:5], v[198:199] op_sel_hi:[1,0]
	v_pk_mul_f32 v[6:7], v[6:7], v[226:227]
	v_pk_mul_f32 v[8:9], v[8:9], v[228:229]
	v_pk_mul_f32 v[2:3], v[2:3], v[230:231]
	v_pk_mul_f32 v[4:5], v[4:5], v[232:233]
	v_mul_f32_e32 v240, 0xbfb8aa3b, v6
	v_mul_f32_e32 v241, 0xbfb8aa3b, v7
	v_mul_f32_e32 v242, 0xbfb8aa3b, v8
	v_mul_f32_e32 v243, 0xbfb8aa3b, v9
	v_mul_f32_e32 v244, 0xbfb8aa3b, v2
	v_mul_f32_e32 v245, 0xbfb8aa3b, v3
	v_mul_f32_e32 v246, 0xbfb8aa3b, v4
	v_mul_f32_e32 v247, 0xbfb8aa3b, v5
	v_exp_f32_e32 v240, v240
	v_exp_f32_e32 v241, v241
	v_exp_f32_e32 v242, v242
	v_exp_f32_e32 v243, v243
	v_exp_f32_e32 v244, v244
	v_exp_f32_e32 v245, v245
	v_exp_f32_e32 v246, v246
	v_exp_f32_e32 v247, v247
	v_add_f32_e32 v240, 1.0, v240
	v_add_f32_e32 v241, 1.0, v241
	v_add_f32_e32 v242, 1.0, v242
	v_add_f32_e32 v243, 1.0, v243
	v_add_f32_e32 v244, 1.0, v244
	v_add_f32_e32 v245, 1.0, v245
	v_add_f32_e32 v246, 1.0, v246
	v_add_f32_e32 v247, 1.0, v247
	v_rcp_f32_e32 v240, v240
	v_rcp_f32_e32 v241, v241
	v_rcp_f32_e32 v242, v242
	v_rcp_f32_e32 v243, v243
	v_rcp_f32_e32 v244, v244
	v_rcp_f32_e32 v245, v245
	v_rcp_f32_e32 v246, v246
	v_rcp_f32_e32 v247, v247
	v_pk_mul_f32 v[6:7], v[6:7], v[240:241]
	v_pk_mul_f32 v[8:9], v[8:9], v[242:243]
	v_pk_mul_f32 v[2:3], v[2:3], v[244:245]
	v_pk_mul_f32 v[4:5], v[4:5], v[246:247]
	v_cvt_pk_bf16_f32 v6, v6, v7
	v_cvt_pk_bf16_f32 v7, v8, v9
	v_cvt_pk_bf16_f32 v8, v2, v3
	v_cvt_pk_bf16_f32 v9, v4, v5
	global_store_dwordx4 v[236:237], v[6:9], off sc1
	s_branch .Lfast_tail
.Lfast_sigm:
	v_lshl_add_u64 v[236:237], v[234:235], 0, s[50:51]
	v_cvt_f32_i32_e32 v142, v142
	v_cvt_f32_i32_e32 v143, v143
	v_cvt_f32_i32_e32 v144, v144
	v_cvt_f32_i32_e32 v145, v145
	v_cvt_f32_i32_e32 v138, v138
	v_cvt_f32_i32_e32 v139, v139
	v_cvt_f32_i32_e32 v140, v140
	v_cvt_f32_i32_e32 v141, v141
	s_waitcnt lgkmcnt(0)
	v_pk_mul_f32 v[142:143], v[142:143], v[208:209] op_sel_hi:[1,0]
	v_pk_mul_f32 v[144:145], v[144:145], v[208:209] op_sel_hi:[1,0]
	v_pk_mul_f32 v[138:139], v[138:139], v[208:209] op_sel_hi:[1,0]
	v_pk_mul_f32 v[140:141], v[140:141], v[208:209] op_sel_hi:[1,0]
	v_pk_mul_f32 v[142:143], v[142:143], v[216:217]
	v_pk_mul_f32 v[144:145], v[144:145], v[218:219]
	v_pk_mul_f32 v[138:139], v[138:139], v[220:221]
	v_pk_mul_f32 v[140:141], v[140:141], v[222:223]
	v_mul_f32_e32 v240, 0xbfb8aa3b, v142
	v_mul_f32_e32 v241, 0xbfb8aa3b, v143
	v_mul_f32_e32 v242, 0xbfb8aa3b, v144
	v_mul_f32_e32 v243, 0xbfb8aa3b, v145
	v_mul_f32_e32 v244, 0xbfb8aa3b, v138
	v_mul_f32_e32 v245, 0xbfb8aa3b, v139
	v_mul_f32_e32 v246, 0xbfb8aa3b, v140
	v_mul_f32_e32 v247, 0xbfb8aa3b, v141
	v_exp_f32_e32 v240, v240
	v_exp_f32_e32 v241, v241
	v_exp_f32_e32 v242, v242
	v_exp_f32_e32 v243, v243
	v_exp_f32_e32 v244, v244
	v_exp_f32_e32 v245, v245
	v_exp_f32_e32 v246, v246
	v_exp_f32_e32 v247, v247
	v_add_f32_e32 v240, 1.0, v240
	v_add_f32_e32 v241, 1.0, v241
	v_add_f32_e32 v242, 1.0, v242
	v_add_f32_e32 v243, 1.0, v243
	v_add_f32_e32 v244, 1.0, v244
	v_add_f32_e32 v245, 1.0, v245
	v_add_f32_e32 v246, 1.0, v246
	v_add_f32_e32 v247, 1.0, v247
	v_rcp_f32_e32 v240, v240
	v_rcp_f32_e32 v241, v241
	v_rcp_f32_e32 v242, v242
	v_rcp_f32_e32 v243, v243
	v_rcp_f32_e32 v244, v244
	v_rcp_f32_e32 v245, v245
	v_rcp_f32_e32 v246, v246
	v_rcp_f32_e32 v247, v247
	s_nop 0
	v_cvt_pk_bf16_f32 v142, v240, v241
	v_cvt_pk_bf16_f32 v143, v242, v243
	v_cvt_pk_bf16_f32 v144, v244, v245
	v_cvt_pk_bf16_f32 v145, v246, v247
	global_store_dwordx4 v[234:235], v[142:145], off sc1
	v_cvt_f32_i32_e32 v134, v134
	v_cvt_f32_i32_e32 v135, v135
	v_cvt_f32_i32_e32 v136, v136
	v_cvt_f32_i32_e32 v137, v137
	v_cvt_f32_i32_e32 v130, v130
	v_cvt_f32_i32_e32 v131, v131
	v_cvt_f32_i32_e32 v132, v132
	v_cvt_f32_i32_e32 v133, v133
	v_pk_mul_f32 v[134:135], v[134:135], v[208:209] op_sel_hi:[1,0]
	v_pk_mul_f32 v[136:137], v[136:137], v[208:209] op_sel_hi:[1,0]
	v_pk_mul_f32 v[130:131], v[130:131], v[208:209] op_sel_hi:[1,0]
	v_pk_mul_f32 v[132:133], v[132:133], v[208:209] op_sel_hi:[1,0]
	v_pk_mul_f32 v[134:135], v[134:135], v[226:227]
	v_pk_mul_f32 v[136:137], v[136:137], v[228:229]
	v_pk_mul_f32 v[130:131], v[130:131], v[230:231]
	v_pk_mul_f32 v[132:133], v[132:133], v[232:233]
	v_mul_f32_e32 v240, 0xbfb8aa3b, v134
	v_mul_f32_e32 v241, 0xbfb8aa3b, v135
	v_mul_f32_e32 v242, 0xbfb8aa3b, v136
	v_mul_f32_e32 v243, 0xbfb8aa3b, v137
	v_mul_f32_e32 v244, 0xbfb8aa3b, v130
	v_mul_f32_e32 v245, 0xbfb8aa3b, v131
	v_mul_f32_e32 v246, 0xbfb8aa3b, v132
	v_mul_f32_e32 v247, 0xbfb8aa3b, v133
	v_exp_f32_e32 v240, v240
	v_exp_f32_e32 v241, v241
	v_exp_f32_e32 v242, v242
	v_exp_f32_e32 v243, v243
	v_exp_f32_e32 v244, v244
	v_exp_f32_e32 v245, v245
	v_exp_f32_e32 v246, v246
	v_exp_f32_e32 v247, v247
	v_add_f32_e32 v240, 1.0, v240
	v_add_f32_e32 v241, 1.0, v241
	v_add_f32_e32 v242, 1.0, v242
	v_add_f32_e32 v243, 1.0, v243
	v_add_f32_e32 v244, 1.0, v244
	v_add_f32_e32 v245, 1.0, v245
	v_add_f32_e32 v246, 1.0, v246
	v_add_f32_e32 v247, 1.0, v247
	v_rcp_f32_e32 v240, v240
	v_rcp_f32_e32 v241, v241
	v_rcp_f32_e32 v242, v242
	v_rcp_f32_e32 v243, v243
	v_rcp_f32_e32 v244, v244
	v_rcp_f32_e32 v245, v245
	v_rcp_f32_e32 v246, v246
	v_rcp_f32_e32 v247, v247
	s_nop 0
	v_cvt_pk_bf16_f32 v134, v240, v241
	v_cvt_pk_bf16_f32 v135, v242, v243
	v_cvt_pk_bf16_f32 v136, v244, v245
	v_cvt_pk_bf16_f32 v137, v246, v247
	global_store_dwordx4 v[236:237], v[134:137], off sc1
	v_lshl_add_u64 v[234:235], v[234:235], 0, s[46:47]
	v_lshl_add_u64 v[236:237], v[234:235], 0, s[50:51]
	v_cvt_f32_i32_e32 v126, v126
	v_cvt_f32_i32_e32 v127, v127
	v_cvt_f32_i32_e32 v128, v128
	v_cvt_f32_i32_e32 v129, v129
	v_cvt_f32_i32_e32 v122, v122
	v_cvt_f32_i32_e32 v123, v123
	v_cvt_f32_i32_e32 v124, v124
	v_cvt_f32_i32_e32 v125, v125
	v_pk_mul_f32 v[126:127], v[126:127], v[210:211] op_sel_hi:[1,0]
	v_pk_mul_f32 v[128:129], v[128:129], v[210:211] op_sel_hi:[1,0]
	v_pk_mul_f32 v[122:123], v[122:123], v[210:211] op_sel_hi:[1,0]
	v_pk_mul_f32 v[124:125], v[124:125], v[210:211] op_sel_hi:[1,0]
	v_pk_mul_f32 v[126:127], v[126:127], v[216:217]
	v_pk_mul_f32 v[128:129], v[128:129], v[218:219]
	v_pk_mul_f32 v[122:123], v[122:123], v[220:221]
	v_pk_mul_f32 v[124:125], v[124:125], v[222:223]
	v_mul_f32_e32 v240, 0xbfb8aa3b, v126
	v_mul_f32_e32 v241, 0xbfb8aa3b, v127
	v_mul_f32_e32 v242, 0xbfb8aa3b, v128
	v_mul_f32_e32 v243, 0xbfb8aa3b, v129
	v_mul_f32_e32 v244, 0xbfb8aa3b, v122
	v_mul_f32_e32 v245, 0xbfb8aa3b, v123
	v_mul_f32_e32 v246, 0xbfb8aa3b, v124
	v_mul_f32_e32 v247, 0xbfb8aa3b, v125
	v_exp_f32_e32 v240, v240
	v_exp_f32_e32 v241, v241
	v_exp_f32_e32 v242, v242
	v_exp_f32_e32 v243, v243
	v_exp_f32_e32 v244, v244
	v_exp_f32_e32 v245, v245
	v_exp_f32_e32 v246, v246
	v_exp_f32_e32 v247, v247
	v_add_f32_e32 v240, 1.0, v240
	v_add_f32_e32 v241, 1.0, v241
	v_add_f32_e32 v242, 1.0, v242
	v_add_f32_e32 v243, 1.0, v243
	v_add_f32_e32 v244, 1.0, v244
	v_add_f32_e32 v245, 1.0, v245
	v_add_f32_e32 v246, 1.0, v246
	v_add_f32_e32 v247, 1.0, v247
	v_rcp_f32_e32 v240, v240
	v_rcp_f32_e32 v241, v241
	v_rcp_f32_e32 v242, v242
	v_rcp_f32_e32 v243, v243
	v_rcp_f32_e32 v244, v244
	v_rcp_f32_e32 v245, v245
	v_rcp_f32_e32 v246, v246
	v_rcp_f32_e32 v247, v247
	s_nop 0
	v_cvt_pk_bf16_f32 v126, v240, v241
	v_cvt_pk_bf16_f32 v127, v242, v243
	v_cvt_pk_bf16_f32 v128, v244, v245
	v_cvt_pk_bf16_f32 v129, v246, v247
	global_store_dwordx4 v[234:235], v[126:129], off sc1
	v_cvt_f32_i32_e32 v118, v118
	v_cvt_f32_i32_e32 v119, v119
	v_cvt_f32_i32_e32 v120, v120
	v_cvt_f32_i32_e32 v121, v121
	v_cvt_f32_i32_e32 v114, v114
	v_cvt_f32_i32_e32 v115, v115
	v_cvt_f32_i32_e32 v116, v116
	v_cvt_f32_i32_e32 v117, v117
	v_pk_mul_f32 v[118:119], v[118:119], v[210:211] op_sel_hi:[1,0]
	v_pk_mul_f32 v[120:121], v[120:121], v[210:211] op_sel_hi:[1,0]
	v_pk_mul_f32 v[114:115], v[114:115], v[210:211] op_sel_hi:[1,0]
	v_pk_mul_f32 v[116:117], v[116:117], v[210:211] op_sel_hi:[1,0]
	v_pk_mul_f32 v[118:119], v[118:119], v[226:227]
	v_pk_mul_f32 v[120:121], v[120:121], v[228:229]
	v_pk_mul_f32 v[114:115], v[114:115], v[230:231]
	v_pk_mul_f32 v[116:117], v[116:117], v[232:233]
	v_mul_f32_e32 v240, 0xbfb8aa3b, v118
	v_mul_f32_e32 v241, 0xbfb8aa3b, v119
	v_mul_f32_e32 v242, 0xbfb8aa3b, v120
	v_mul_f32_e32 v243, 0xbfb8aa3b, v121
	v_mul_f32_e32 v244, 0xbfb8aa3b, v114
	v_mul_f32_e32 v245, 0xbfb8aa3b, v115
	v_mul_f32_e32 v246, 0xbfb8aa3b, v116
	v_mul_f32_e32 v247, 0xbfb8aa3b, v117
	v_exp_f32_e32 v240, v240
	v_exp_f32_e32 v241, v241
	v_exp_f32_e32 v242, v242
	v_exp_f32_e32 v243, v243
	v_exp_f32_e32 v244, v244
	v_exp_f32_e32 v245, v245
	v_exp_f32_e32 v246, v246
	v_exp_f32_e32 v247, v247
	v_add_f32_e32 v240, 1.0, v240
	v_add_f32_e32 v241, 1.0, v241
	v_add_f32_e32 v242, 1.0, v242
	v_add_f32_e32 v243, 1.0, v243
	v_add_f32_e32 v244, 1.0, v244
	v_add_f32_e32 v245, 1.0, v245
	v_add_f32_e32 v246, 1.0, v246
	v_add_f32_e32 v247, 1.0, v247
	v_rcp_f32_e32 v240, v240
	v_rcp_f32_e32 v241, v241
	v_rcp_f32_e32 v242, v242
	v_rcp_f32_e32 v243, v243
	v_rcp_f32_e32 v244, v244
	v_rcp_f32_e32 v245, v245
	v_rcp_f32_e32 v246, v246
	v_rcp_f32_e32 v247, v247
	s_nop 0
	v_cvt_pk_bf16_f32 v118, v240, v241
	v_cvt_pk_bf16_f32 v119, v242, v243
	v_cvt_pk_bf16_f32 v120, v244, v245
	v_cvt_pk_bf16_f32 v121, v246, v247
	global_store_dwordx4 v[236:237], v[118:121], off sc1
	v_lshl_add_u64 v[234:235], v[234:235], 0, s[46:47]
	v_lshl_add_u64 v[236:237], v[234:235], 0, s[50:51]
	v_cvt_f32_i32_e32 v110, v110
	v_cvt_f32_i32_e32 v111, v111
	v_cvt_f32_i32_e32 v112, v112
	v_cvt_f32_i32_e32 v113, v113
	v_cvt_f32_i32_e32 v106, v106
	v_cvt_f32_i32_e32 v107, v107
	v_cvt_f32_i32_e32 v108, v108
	v_cvt_f32_i32_e32 v109, v109
	v_pk_mul_f32 v[110:111], v[110:111], v[212:213] op_sel_hi:[1,0]
	v_pk_mul_f32 v[112:113], v[112:113], v[212:213] op_sel_hi:[1,0]
	v_pk_mul_f32 v[106:107], v[106:107], v[212:213] op_sel_hi:[1,0]
	v_pk_mul_f32 v[108:109], v[108:109], v[212:213] op_sel_hi:[1,0]
	v_pk_mul_f32 v[110:111], v[110:111], v[216:217]
	v_pk_mul_f32 v[112:113], v[112:113], v[218:219]
	v_pk_mul_f32 v[106:107], v[106:107], v[220:221]
	v_pk_mul_f32 v[108:109], v[108:109], v[222:223]
	v_mul_f32_e32 v240, 0xbfb8aa3b, v110
	v_mul_f32_e32 v241, 0xbfb8aa3b, v111
	v_mul_f32_e32 v242, 0xbfb8aa3b, v112
	v_mul_f32_e32 v243, 0xbfb8aa3b, v113
	v_mul_f32_e32 v244, 0xbfb8aa3b, v106
	v_mul_f32_e32 v245, 0xbfb8aa3b, v107
	v_mul_f32_e32 v246, 0xbfb8aa3b, v108
	v_mul_f32_e32 v247, 0xbfb8aa3b, v109
	v_exp_f32_e32 v240, v240
	v_exp_f32_e32 v241, v241
	v_exp_f32_e32 v242, v242
	v_exp_f32_e32 v243, v243
	v_exp_f32_e32 v244, v244
	v_exp_f32_e32 v245, v245
	v_exp_f32_e32 v246, v246
	v_exp_f32_e32 v247, v247
	v_add_f32_e32 v240, 1.0, v240
	v_add_f32_e32 v241, 1.0, v241
	v_add_f32_e32 v242, 1.0, v242
	v_add_f32_e32 v243, 1.0, v243
	v_add_f32_e32 v244, 1.0, v244
	v_add_f32_e32 v245, 1.0, v245
	v_add_f32_e32 v246, 1.0, v246
	v_add_f32_e32 v247, 1.0, v247
	v_rcp_f32_e32 v240, v240
	v_rcp_f32_e32 v241, v241
	v_rcp_f32_e32 v242, v242
	v_rcp_f32_e32 v243, v243
	v_rcp_f32_e32 v244, v244
	v_rcp_f32_e32 v245, v245
	v_rcp_f32_e32 v246, v246
	v_rcp_f32_e32 v247, v247
	s_nop 0
	v_cvt_pk_bf16_f32 v110, v240, v241
	v_cvt_pk_bf16_f32 v111, v242, v243
	v_cvt_pk_bf16_f32 v112, v244, v245
	v_cvt_pk_bf16_f32 v113, v246, v247
	global_store_dwordx4 v[234:235], v[110:113], off sc1
	v_cvt_f32_i32_e32 v102, v102
	v_cvt_f32_i32_e32 v103, v103
	v_cvt_f32_i32_e32 v104, v104
	v_cvt_f32_i32_e32 v105, v105
	v_cvt_f32_i32_e32 v98, v98
	v_cvt_f32_i32_e32 v99, v99
	v_cvt_f32_i32_e32 v100, v100
	v_cvt_f32_i32_e32 v101, v101
	v_pk_mul_f32 v[102:103], v[102:103], v[212:213] op_sel_hi:[1,0]
	v_pk_mul_f32 v[104:105], v[104:105], v[212:213] op_sel_hi:[1,0]
	v_pk_mul_f32 v[98:99], v[98:99], v[212:213] op_sel_hi:[1,0]
	v_pk_mul_f32 v[100:101], v[100:101], v[212:213] op_sel_hi:[1,0]
	v_pk_mul_f32 v[102:103], v[102:103], v[226:227]
	v_pk_mul_f32 v[104:105], v[104:105], v[228:229]
	v_pk_mul_f32 v[98:99], v[98:99], v[230:231]
	v_pk_mul_f32 v[100:101], v[100:101], v[232:233]
	v_mul_f32_e32 v240, 0xbfb8aa3b, v102
	v_mul_f32_e32 v241, 0xbfb8aa3b, v103
	v_mul_f32_e32 v242, 0xbfb8aa3b, v104
	v_mul_f32_e32 v243, 0xbfb8aa3b, v105
	v_mul_f32_e32 v244, 0xbfb8aa3b, v98
	v_mul_f32_e32 v245, 0xbfb8aa3b, v99
	v_mul_f32_e32 v246, 0xbfb8aa3b, v100
	v_mul_f32_e32 v247, 0xbfb8aa3b, v101
	v_exp_f32_e32 v240, v240
	v_exp_f32_e32 v241, v241
	v_exp_f32_e32 v242, v242
	v_exp_f32_e32 v243, v243
	v_exp_f32_e32 v244, v244
	v_exp_f32_e32 v245, v245
	v_exp_f32_e32 v246, v246
	v_exp_f32_e32 v247, v247
	v_add_f32_e32 v240, 1.0, v240
	v_add_f32_e32 v241, 1.0, v241
	v_add_f32_e32 v242, 1.0, v242
	v_add_f32_e32 v243, 1.0, v243
	v_add_f32_e32 v244, 1.0, v244
	v_add_f32_e32 v245, 1.0, v245
	v_add_f32_e32 v246, 1.0, v246
	v_add_f32_e32 v247, 1.0, v247
	v_rcp_f32_e32 v240, v240
	v_rcp_f32_e32 v241, v241
	v_rcp_f32_e32 v242, v242
	v_rcp_f32_e32 v243, v243
	v_rcp_f32_e32 v244, v244
	v_rcp_f32_e32 v245, v245
	v_rcp_f32_e32 v246, v246
	v_rcp_f32_e32 v247, v247
	s_nop 0
	v_cvt_pk_bf16_f32 v102, v240, v241
	v_cvt_pk_bf16_f32 v103, v242, v243
	v_cvt_pk_bf16_f32 v104, v244, v245
	v_cvt_pk_bf16_f32 v105, v246, v247
	global_store_dwordx4 v[236:237], v[102:105], off sc1
	v_lshl_add_u64 v[234:235], v[234:235], 0, s[46:47]
	v_lshl_add_u64 v[236:237], v[234:235], 0, s[50:51]
	v_cvt_f32_i32_e32 v94, v94
	v_cvt_f32_i32_e32 v95, v95
	v_cvt_f32_i32_e32 v96, v96
	v_cvt_f32_i32_e32 v97, v97
	v_cvt_f32_i32_e32 v90, v90
	v_cvt_f32_i32_e32 v91, v91
	v_cvt_f32_i32_e32 v92, v92
	v_cvt_f32_i32_e32 v93, v93
	v_pk_mul_f32 v[94:95], v[94:95], v[214:215] op_sel_hi:[1,0]
	v_pk_mul_f32 v[96:97], v[96:97], v[214:215] op_sel_hi:[1,0]
	v_pk_mul_f32 v[90:91], v[90:91], v[214:215] op_sel_hi:[1,0]
	v_pk_mul_f32 v[92:93], v[92:93], v[214:215] op_sel_hi:[1,0]
	v_pk_mul_f32 v[94:95], v[94:95], v[216:217]
	v_pk_mul_f32 v[96:97], v[96:97], v[218:219]
	v_pk_mul_f32 v[90:91], v[90:91], v[220:221]
	v_pk_mul_f32 v[92:93], v[92:93], v[222:223]
	v_mul_f32_e32 v240, 0xbfb8aa3b, v94
	v_mul_f32_e32 v241, 0xbfb8aa3b, v95
	v_mul_f32_e32 v242, 0xbfb8aa3b, v96
	v_mul_f32_e32 v243, 0xbfb8aa3b, v97
	v_mul_f32_e32 v244, 0xbfb8aa3b, v90
	v_mul_f32_e32 v245, 0xbfb8aa3b, v91
	v_mul_f32_e32 v246, 0xbfb8aa3b, v92
	v_mul_f32_e32 v247, 0xbfb8aa3b, v93
	v_exp_f32_e32 v240, v240
	v_exp_f32_e32 v241, v241
	v_exp_f32_e32 v242, v242
	v_exp_f32_e32 v243, v243
	v_exp_f32_e32 v244, v244
	v_exp_f32_e32 v245, v245
	v_exp_f32_e32 v246, v246
	v_exp_f32_e32 v247, v247
	v_add_f32_e32 v240, 1.0, v240
	v_add_f32_e32 v241, 1.0, v241
	v_add_f32_e32 v242, 1.0, v242
	v_add_f32_e32 v243, 1.0, v243
	v_add_f32_e32 v244, 1.0, v244
	v_add_f32_e32 v245, 1.0, v245
	v_add_f32_e32 v246, 1.0, v246
	v_add_f32_e32 v247, 1.0, v247
	v_rcp_f32_e32 v240, v240
	v_rcp_f32_e32 v241, v241
	v_rcp_f32_e32 v242, v242
	v_rcp_f32_e32 v243, v243
	v_rcp_f32_e32 v244, v244
	v_rcp_f32_e32 v245, v245
	v_rcp_f32_e32 v246, v246
	v_rcp_f32_e32 v247, v247
	s_nop 0
	v_cvt_pk_bf16_f32 v94, v240, v241
	v_cvt_pk_bf16_f32 v95, v242, v243
	v_cvt_pk_bf16_f32 v96, v244, v245
	v_cvt_pk_bf16_f32 v97, v246, v247
	global_store_dwordx4 v[234:235], v[94:97], off sc1
	v_cvt_f32_i32_e32 v86, v86
	v_cvt_f32_i32_e32 v87, v87
	v_cvt_f32_i32_e32 v88, v88
	v_cvt_f32_i32_e32 v89, v89
	v_cvt_f32_i32_e32 v82, v82
	v_cvt_f32_i32_e32 v83, v83
	v_cvt_f32_i32_e32 v84, v84
	v_cvt_f32_i32_e32 v85, v85
	v_pk_mul_f32 v[86:87], v[86:87], v[214:215] op_sel_hi:[1,0]
	v_pk_mul_f32 v[88:89], v[88:89], v[214:215] op_sel_hi:[1,0]
	v_pk_mul_f32 v[82:83], v[82:83], v[214:215] op_sel_hi:[1,0]
	v_pk_mul_f32 v[84:85], v[84:85], v[214:215] op_sel_hi:[1,0]
	v_pk_mul_f32 v[86:87], v[86:87], v[226:227]
	v_pk_mul_f32 v[88:89], v[88:89], v[228:229]
	v_pk_mul_f32 v[82:83], v[82:83], v[230:231]
	v_pk_mul_f32 v[84:85], v[84:85], v[232:233]
	v_mul_f32_e32 v240, 0xbfb8aa3b, v86
	v_mul_f32_e32 v241, 0xbfb8aa3b, v87
	v_mul_f32_e32 v242, 0xbfb8aa3b, v88
	v_mul_f32_e32 v243, 0xbfb8aa3b, v89
	v_mul_f32_e32 v244, 0xbfb8aa3b, v82
	v_mul_f32_e32 v245, 0xbfb8aa3b, v83
	v_mul_f32_e32 v246, 0xbfb8aa3b, v84
	v_mul_f32_e32 v247, 0xbfb8aa3b, v85
	v_exp_f32_e32 v240, v240
	v_exp_f32_e32 v241, v241
	v_exp_f32_e32 v242, v242
	v_exp_f32_e32 v243, v243
	v_exp_f32_e32 v244, v244
	v_exp_f32_e32 v245, v245
	v_exp_f32_e32 v246, v246
	v_exp_f32_e32 v247, v247
	v_add_f32_e32 v240, 1.0, v240
	v_add_f32_e32 v241, 1.0, v241
	v_add_f32_e32 v242, 1.0, v242
	v_add_f32_e32 v243, 1.0, v243
	v_add_f32_e32 v244, 1.0, v244
	v_add_f32_e32 v245, 1.0, v245
	v_add_f32_e32 v246, 1.0, v246
	v_add_f32_e32 v247, 1.0, v247
	v_rcp_f32_e32 v240, v240
	v_rcp_f32_e32 v241, v241
	v_rcp_f32_e32 v242, v242
	v_rcp_f32_e32 v243, v243
	v_rcp_f32_e32 v244, v244
	v_rcp_f32_e32 v245, v245
	v_rcp_f32_e32 v246, v246
	v_rcp_f32_e32 v247, v247
	s_nop 0
	v_cvt_pk_bf16_f32 v86, v240, v241
	v_cvt_pk_bf16_f32 v87, v242, v243
	v_cvt_pk_bf16_f32 v88, v244, v245
	v_cvt_pk_bf16_f32 v89, v246, v247
	global_store_dwordx4 v[236:237], v[86:89], off sc1
	v_lshl_add_u64 v[234:235], v[234:235], 0, s[48:49]
	v_lshl_add_u64 v[236:237], v[234:235], 0, s[50:51]
	v_cvt_f32_i32_e32 v78, v78
	v_cvt_f32_i32_e32 v79, v79
	v_cvt_f32_i32_e32 v80, v80
	v_cvt_f32_i32_e32 v81, v81
	v_cvt_f32_i32_e32 v74, v74
	v_cvt_f32_i32_e32 v75, v75
	v_cvt_f32_i32_e32 v76, v76
	v_cvt_f32_i32_e32 v77, v77
	v_pk_mul_f32 v[78:79], v[78:79], v[178:179] op_sel_hi:[1,0]
	v_pk_mul_f32 v[80:81], v[80:81], v[178:179] op_sel_hi:[1,0]
	v_pk_mul_f32 v[74:75], v[74:75], v[178:179] op_sel_hi:[1,0]
	v_pk_mul_f32 v[76:77], v[76:77], v[178:179] op_sel_hi:[1,0]
	v_pk_mul_f32 v[78:79], v[78:79], v[216:217]
	v_pk_mul_f32 v[80:81], v[80:81], v[218:219]
	v_pk_mul_f32 v[74:75], v[74:75], v[220:221]
	v_pk_mul_f32 v[76:77], v[76:77], v[222:223]
	v_mul_f32_e32 v240, 0xbfb8aa3b, v78
	v_mul_f32_e32 v241, 0xbfb8aa3b, v79
	v_mul_f32_e32 v242, 0xbfb8aa3b, v80
	v_mul_f32_e32 v243, 0xbfb8aa3b, v81
	v_mul_f32_e32 v244, 0xbfb8aa3b, v74
	v_mul_f32_e32 v245, 0xbfb8aa3b, v75
	v_mul_f32_e32 v246, 0xbfb8aa3b, v76
	v_mul_f32_e32 v247, 0xbfb8aa3b, v77
	v_exp_f32_e32 v240, v240
	v_exp_f32_e32 v241, v241
	v_exp_f32_e32 v242, v242
	v_exp_f32_e32 v243, v243
	v_exp_f32_e32 v244, v244
	v_exp_f32_e32 v245, v245
	v_exp_f32_e32 v246, v246
	v_exp_f32_e32 v247, v247
	v_add_f32_e32 v240, 1.0, v240
	v_add_f32_e32 v241, 1.0, v241
	v_add_f32_e32 v242, 1.0, v242
	v_add_f32_e32 v243, 1.0, v243
	v_add_f32_e32 v244, 1.0, v244
	v_add_f32_e32 v245, 1.0, v245
	v_add_f32_e32 v246, 1.0, v246
	v_add_f32_e32 v247, 1.0, v247
	v_rcp_f32_e32 v240, v240
	v_rcp_f32_e32 v241, v241
	v_rcp_f32_e32 v242, v242
	v_rcp_f32_e32 v243, v243
	v_rcp_f32_e32 v244, v244
	v_rcp_f32_e32 v245, v245
	v_rcp_f32_e32 v246, v246
	v_rcp_f32_e32 v247, v247
	s_nop 0
	v_cvt_pk_bf16_f32 v78, v240, v241
	v_cvt_pk_bf16_f32 v79, v242, v243
	v_cvt_pk_bf16_f32 v80, v244, v245
	v_cvt_pk_bf16_f32 v81, v246, v247
	global_store_dwordx4 v[234:235], v[78:81], off sc1
	v_cvt_f32_i32_e32 v70, v70
	v_cvt_f32_i32_e32 v71, v71
	v_cvt_f32_i32_e32 v72, v72
	v_cvt_f32_i32_e32 v73, v73
	v_cvt_f32_i32_e32 v66, v66
	v_cvt_f32_i32_e32 v67, v67
	v_cvt_f32_i32_e32 v68, v68
	v_cvt_f32_i32_e32 v69, v69
	v_pk_mul_f32 v[70:71], v[70:71], v[178:179] op_sel_hi:[1,0]
	v_pk_mul_f32 v[72:73], v[72:73], v[178:179] op_sel_hi:[1,0]
	v_pk_mul_f32 v[66:67], v[66:67], v[178:179] op_sel_hi:[1,0]
	v_pk_mul_f32 v[68:69], v[68:69], v[178:179] op_sel_hi:[1,0]
	v_pk_mul_f32 v[70:71], v[70:71], v[226:227]
	v_pk_mul_f32 v[72:73], v[72:73], v[228:229]
	v_pk_mul_f32 v[66:67], v[66:67], v[230:231]
	v_pk_mul_f32 v[68:69], v[68:69], v[232:233]
	v_mul_f32_e32 v240, 0xbfb8aa3b, v70
	v_mul_f32_e32 v241, 0xbfb8aa3b, v71
	v_mul_f32_e32 v242, 0xbfb8aa3b, v72
	v_mul_f32_e32 v243, 0xbfb8aa3b, v73
	v_mul_f32_e32 v244, 0xbfb8aa3b, v66
	v_mul_f32_e32 v245, 0xbfb8aa3b, v67
	v_mul_f32_e32 v246, 0xbfb8aa3b, v68
	v_mul_f32_e32 v247, 0xbfb8aa3b, v69
	v_exp_f32_e32 v240, v240
	v_exp_f32_e32 v241, v241
	v_exp_f32_e32 v242, v242
	v_exp_f32_e32 v243, v243
	v_exp_f32_e32 v244, v244
	v_exp_f32_e32 v245, v245
	v_exp_f32_e32 v246, v246
	v_exp_f32_e32 v247, v247
	v_add_f32_e32 v240, 1.0, v240
	v_add_f32_e32 v241, 1.0, v241
	v_add_f32_e32 v242, 1.0, v242
	v_add_f32_e32 v243, 1.0, v243
	v_add_f32_e32 v244, 1.0, v244
	v_add_f32_e32 v245, 1.0, v245
	v_add_f32_e32 v246, 1.0, v246
	v_add_f32_e32 v247, 1.0, v247
	v_rcp_f32_e32 v240, v240
	v_rcp_f32_e32 v241, v241
	v_rcp_f32_e32 v242, v242
	v_rcp_f32_e32 v243, v243
	v_rcp_f32_e32 v244, v244
	v_rcp_f32_e32 v245, v245
	v_rcp_f32_e32 v246, v246
	v_rcp_f32_e32 v247, v247
	s_nop 0
	v_cvt_pk_bf16_f32 v70, v240, v241
	v_cvt_pk_bf16_f32 v71, v242, v243
	v_cvt_pk_bf16_f32 v72, v244, v245
	v_cvt_pk_bf16_f32 v73, v246, v247
	global_store_dwordx4 v[236:237], v[70:73], off sc1
	v_lshl_add_u64 v[234:235], v[234:235], 0, s[46:47]
	v_lshl_add_u64 v[236:237], v[234:235], 0, s[50:51]
	v_cvt_f32_i32_e32 v62, v62
	v_cvt_f32_i32_e32 v63, v63
	v_cvt_f32_i32_e32 v64, v64
	v_cvt_f32_i32_e32 v65, v65
	v_cvt_f32_i32_e32 v58, v58
	v_cvt_f32_i32_e32 v59, v59
	v_cvt_f32_i32_e32 v60, v60
	v_cvt_f32_i32_e32 v61, v61
	v_pk_mul_f32 v[62:63], v[62:63], v[180:181] op_sel_hi:[1,0]
	v_pk_mul_f32 v[64:65], v[64:65], v[180:181] op_sel_hi:[1,0]
	v_pk_mul_f32 v[58:59], v[58:59], v[180:181] op_sel_hi:[1,0]
	v_pk_mul_f32 v[60:61], v[60:61], v[180:181] op_sel_hi:[1,0]
	v_pk_mul_f32 v[62:63], v[62:63], v[216:217]
	v_pk_mul_f32 v[64:65], v[64:65], v[218:219]
	v_pk_mul_f32 v[58:59], v[58:59], v[220:221]
	v_pk_mul_f32 v[60:61], v[60:61], v[222:223]
	v_mul_f32_e32 v240, 0xbfb8aa3b, v62
	v_mul_f32_e32 v241, 0xbfb8aa3b, v63
	v_mul_f32_e32 v242, 0xbfb8aa3b, v64
	v_mul_f32_e32 v243, 0xbfb8aa3b, v65
	v_mul_f32_e32 v244, 0xbfb8aa3b, v58
	v_mul_f32_e32 v245, 0xbfb8aa3b, v59
	v_mul_f32_e32 v246, 0xbfb8aa3b, v60
	v_mul_f32_e32 v247, 0xbfb8aa3b, v61
	v_exp_f32_e32 v240, v240
	v_exp_f32_e32 v241, v241
	v_exp_f32_e32 v242, v242
	v_exp_f32_e32 v243, v243
	v_exp_f32_e32 v244, v244
	v_exp_f32_e32 v245, v245
	v_exp_f32_e32 v246, v246
	v_exp_f32_e32 v247, v247
	v_add_f32_e32 v240, 1.0, v240
	v_add_f32_e32 v241, 1.0, v241
	v_add_f32_e32 v242, 1.0, v242
	v_add_f32_e32 v243, 1.0, v243
	v_add_f32_e32 v244, 1.0, v244
	v_add_f32_e32 v245, 1.0, v245
	v_add_f32_e32 v246, 1.0, v246
	v_add_f32_e32 v247, 1.0, v247
	v_rcp_f32_e32 v240, v240
	v_rcp_f32_e32 v241, v241
	v_rcp_f32_e32 v242, v242
	v_rcp_f32_e32 v243, v243
	v_rcp_f32_e32 v244, v244
	v_rcp_f32_e32 v245, v245
	v_rcp_f32_e32 v246, v246
	v_rcp_f32_e32 v247, v247
	s_nop 0
	v_cvt_pk_bf16_f32 v62, v240, v241
	v_cvt_pk_bf16_f32 v63, v242, v243
	v_cvt_pk_bf16_f32 v64, v244, v245
	v_cvt_pk_bf16_f32 v65, v246, v247
	global_store_dwordx4 v[234:235], v[62:65], off sc1
	v_cvt_f32_i32_e32 v54, v54
	v_cvt_f32_i32_e32 v55, v55
	v_cvt_f32_i32_e32 v56, v56
	v_cvt_f32_i32_e32 v57, v57
	v_cvt_f32_i32_e32 v50, v50
	v_cvt_f32_i32_e32 v51, v51
	v_cvt_f32_i32_e32 v52, v52
	v_cvt_f32_i32_e32 v53, v53
	v_pk_mul_f32 v[54:55], v[54:55], v[180:181] op_sel_hi:[1,0]
	v_pk_mul_f32 v[56:57], v[56:57], v[180:181] op_sel_hi:[1,0]
	v_pk_mul_f32 v[50:51], v[50:51], v[180:181] op_sel_hi:[1,0]
	v_pk_mul_f32 v[52:53], v[52:53], v[180:181] op_sel_hi:[1,0]
	v_pk_mul_f32 v[54:55], v[54:55], v[226:227]
	v_pk_mul_f32 v[56:57], v[56:57], v[228:229]
	v_pk_mul_f32 v[50:51], v[50:51], v[230:231]
	v_pk_mul_f32 v[52:53], v[52:53], v[232:233]
	v_mul_f32_e32 v240, 0xbfb8aa3b, v54
	v_mul_f32_e32 v241, 0xbfb8aa3b, v55
	v_mul_f32_e32 v242, 0xbfb8aa3b, v56
	v_mul_f32_e32 v243, 0xbfb8aa3b, v57
	v_mul_f32_e32 v244, 0xbfb8aa3b, v50
	v_mul_f32_e32 v245, 0xbfb8aa3b, v51
	v_mul_f32_e32 v246, 0xbfb8aa3b, v52
	v_mul_f32_e32 v247, 0xbfb8aa3b, v53
	v_exp_f32_e32 v240, v240
	v_exp_f32_e32 v241, v241
	v_exp_f32_e32 v242, v242
	v_exp_f32_e32 v243, v243
	v_exp_f32_e32 v244, v244
	v_exp_f32_e32 v245, v245
	v_exp_f32_e32 v246, v246
	v_exp_f32_e32 v247, v247
	v_add_f32_e32 v240, 1.0, v240
	v_add_f32_e32 v241, 1.0, v241
	v_add_f32_e32 v242, 1.0, v242
	v_add_f32_e32 v243, 1.0, v243
	v_add_f32_e32 v244, 1.0, v244
	v_add_f32_e32 v245, 1.0, v245
	v_add_f32_e32 v246, 1.0, v246
	v_add_f32_e32 v247, 1.0, v247
	v_rcp_f32_e32 v240, v240
	v_rcp_f32_e32 v241, v241
	v_rcp_f32_e32 v242, v242
	v_rcp_f32_e32 v243, v243
	v_rcp_f32_e32 v244, v244
	v_rcp_f32_e32 v245, v245
	v_rcp_f32_e32 v246, v246
	v_rcp_f32_e32 v247, v247
	s_nop 0
	v_cvt_pk_bf16_f32 v54, v240, v241
	v_cvt_pk_bf16_f32 v55, v242, v243
	v_cvt_pk_bf16_f32 v56, v244, v245
	v_cvt_pk_bf16_f32 v57, v246, v247
	global_store_dwordx4 v[236:237], v[54:57], off sc1
	v_lshl_add_u64 v[234:235], v[234:235], 0, s[46:47]
	v_lshl_add_u64 v[236:237], v[234:235], 0, s[50:51]
	v_cvt_f32_i32_e32 v46, v46
	v_cvt_f32_i32_e32 v47, v47
	v_cvt_f32_i32_e32 v48, v48
	v_cvt_f32_i32_e32 v49, v49
	v_cvt_f32_i32_e32 v42, v42
	v_cvt_f32_i32_e32 v43, v43
	v_cvt_f32_i32_e32 v44, v44
	v_cvt_f32_i32_e32 v45, v45
	v_pk_mul_f32 v[46:47], v[46:47], v[196:197] op_sel_hi:[1,0]
	v_pk_mul_f32 v[48:49], v[48:49], v[196:197] op_sel_hi:[1,0]
	v_pk_mul_f32 v[42:43], v[42:43], v[196:197] op_sel_hi:[1,0]
	v_pk_mul_f32 v[44:45], v[44:45], v[196:197] op_sel_hi:[1,0]
	v_pk_mul_f32 v[46:47], v[46:47], v[216:217]
	v_pk_mul_f32 v[48:49], v[48:49], v[218:219]
	v_pk_mul_f32 v[42:43], v[42:43], v[220:221]
	v_pk_mul_f32 v[44:45], v[44:45], v[222:223]
	v_mul_f32_e32 v240, 0xbfb8aa3b, v46
	v_mul_f32_e32 v241, 0xbfb8aa3b, v47
	v_mul_f32_e32 v242, 0xbfb8aa3b, v48
	v_mul_f32_e32 v243, 0xbfb8aa3b, v49
	v_mul_f32_e32 v244, 0xbfb8aa3b, v42
	v_mul_f32_e32 v245, 0xbfb8aa3b, v43
	v_mul_f32_e32 v246, 0xbfb8aa3b, v44
	v_mul_f32_e32 v247, 0xbfb8aa3b, v45
	v_exp_f32_e32 v240, v240
	v_exp_f32_e32 v241, v241
	v_exp_f32_e32 v242, v242
	v_exp_f32_e32 v243, v243
	v_exp_f32_e32 v244, v244
	v_exp_f32_e32 v245, v245
	v_exp_f32_e32 v246, v246
	v_exp_f32_e32 v247, v247
	v_add_f32_e32 v240, 1.0, v240
	v_add_f32_e32 v241, 1.0, v241
	v_add_f32_e32 v242, 1.0, v242
	v_add_f32_e32 v243, 1.0, v243
	v_add_f32_e32 v244, 1.0, v244
	v_add_f32_e32 v245, 1.0, v245
	v_add_f32_e32 v246, 1.0, v246
	v_add_f32_e32 v247, 1.0, v247
	v_rcp_f32_e32 v240, v240
	v_rcp_f32_e32 v241, v241
	v_rcp_f32_e32 v242, v242
	v_rcp_f32_e32 v243, v243
	v_rcp_f32_e32 v244, v244
	v_rcp_f32_e32 v245, v245
	v_rcp_f32_e32 v246, v246
	v_rcp_f32_e32 v247, v247
	s_nop 0
	v_cvt_pk_bf16_f32 v46, v240, v241
	v_cvt_pk_bf16_f32 v47, v242, v243
	v_cvt_pk_bf16_f32 v48, v244, v245
	v_cvt_pk_bf16_f32 v49, v246, v247
	global_store_dwordx4 v[234:235], v[46:49], off sc1
	v_cvt_f32_i32_e32 v30, v30
	v_cvt_f32_i32_e32 v31, v31
	v_cvt_f32_i32_e32 v32, v32
	v_cvt_f32_i32_e32 v33, v33
	v_cvt_f32_i32_e32 v26, v26
	v_cvt_f32_i32_e32 v27, v27
	v_cvt_f32_i32_e32 v28, v28
	v_cvt_f32_i32_e32 v29, v29
	v_pk_mul_f32 v[30:31], v[30:31], v[196:197] op_sel_hi:[1,0]
	v_pk_mul_f32 v[32:33], v[32:33], v[196:197] op_sel_hi:[1,0]
	v_pk_mul_f32 v[26:27], v[26:27], v[196:197] op_sel_hi:[1,0]
	v_pk_mul_f32 v[28:29], v[28:29], v[196:197] op_sel_hi:[1,0]
	v_pk_mul_f32 v[30:31], v[30:31], v[226:227]
	v_pk_mul_f32 v[32:33], v[32:33], v[228:229]
	v_pk_mul_f32 v[26:27], v[26:27], v[230:231]
	v_pk_mul_f32 v[28:29], v[28:29], v[232:233]
	v_mul_f32_e32 v240, 0xbfb8aa3b, v30
	v_mul_f32_e32 v241, 0xbfb8aa3b, v31
	v_mul_f32_e32 v242, 0xbfb8aa3b, v32
	v_mul_f32_e32 v243, 0xbfb8aa3b, v33
	v_mul_f32_e32 v244, 0xbfb8aa3b, v26
	v_mul_f32_e32 v245, 0xbfb8aa3b, v27
	v_mul_f32_e32 v246, 0xbfb8aa3b, v28
	v_mul_f32_e32 v247, 0xbfb8aa3b, v29
	v_exp_f32_e32 v240, v240
	v_exp_f32_e32 v241, v241
	v_exp_f32_e32 v242, v242
	v_exp_f32_e32 v243, v243
	v_exp_f32_e32 v244, v244
	v_exp_f32_e32 v245, v245
	v_exp_f32_e32 v246, v246
	v_exp_f32_e32 v247, v247
	v_add_f32_e32 v240, 1.0, v240
	v_add_f32_e32 v241, 1.0, v241
	v_add_f32_e32 v242, 1.0, v242
	v_add_f32_e32 v243, 1.0, v243
	v_add_f32_e32 v244, 1.0, v244
	v_add_f32_e32 v245, 1.0, v245
	v_add_f32_e32 v246, 1.0, v246
	v_add_f32_e32 v247, 1.0, v247
	v_rcp_f32_e32 v240, v240
	v_rcp_f32_e32 v241, v241
	v_rcp_f32_e32 v242, v242
	v_rcp_f32_e32 v243, v243
	v_rcp_f32_e32 v244, v244
	v_rcp_f32_e32 v245, v245
	v_rcp_f32_e32 v246, v246
	v_rcp_f32_e32 v247, v247
	s_nop 0
	v_cvt_pk_bf16_f32 v30, v240, v241
	v_cvt_pk_bf16_f32 v31, v242, v243
	v_cvt_pk_bf16_f32 v32, v244, v245
	v_cvt_pk_bf16_f32 v33, v246, v247
	global_store_dwordx4 v[236:237], v[30:33], off sc1
	v_lshl_add_u64 v[234:235], v[234:235], 0, s[46:47]
	v_lshl_add_u64 v[236:237], v[234:235], 0, s[50:51]
	v_cvt_f32_i32_e32 v14, v14
	v_cvt_f32_i32_e32 v15, v15
	v_cvt_f32_i32_e32 v16, v16
	v_cvt_f32_i32_e32 v17, v17
	v_cvt_f32_i32_e32 v10, v10
	v_cvt_f32_i32_e32 v11, v11
	v_cvt_f32_i32_e32 v12, v12
	v_cvt_f32_i32_e32 v13, v13
	v_pk_mul_f32 v[14:15], v[14:15], v[198:199] op_sel_hi:[1,0]
	v_pk_mul_f32 v[16:17], v[16:17], v[198:199] op_sel_hi:[1,0]
	v_pk_mul_f32 v[10:11], v[10:11], v[198:199] op_sel_hi:[1,0]
	v_pk_mul_f32 v[12:13], v[12:13], v[198:199] op_sel_hi:[1,0]
	v_pk_mul_f32 v[14:15], v[14:15], v[216:217]
	v_pk_mul_f32 v[16:17], v[16:17], v[218:219]
	v_pk_mul_f32 v[10:11], v[10:11], v[220:221]
	v_pk_mul_f32 v[12:13], v[12:13], v[222:223]
	v_mul_f32_e32 v240, 0xbfb8aa3b, v14
	v_mul_f32_e32 v241, 0xbfb8aa3b, v15
	v_mul_f32_e32 v242, 0xbfb8aa3b, v16
	v_mul_f32_e32 v243, 0xbfb8aa3b, v17
	v_mul_f32_e32 v244, 0xbfb8aa3b, v10
	v_mul_f32_e32 v245, 0xbfb8aa3b, v11
	v_mul_f32_e32 v246, 0xbfb8aa3b, v12
	v_mul_f32_e32 v247, 0xbfb8aa3b, v13
	v_exp_f32_e32 v240, v240
	v_exp_f32_e32 v241, v241
	v_exp_f32_e32 v242, v242
	v_exp_f32_e32 v243, v243
	v_exp_f32_e32 v244, v244
	v_exp_f32_e32 v245, v245
	v_exp_f32_e32 v246, v246
	v_exp_f32_e32 v247, v247
	v_add_f32_e32 v240, 1.0, v240
	v_add_f32_e32 v241, 1.0, v241
	v_add_f32_e32 v242, 1.0, v242
	v_add_f32_e32 v243, 1.0, v243
	v_add_f32_e32 v244, 1.0, v244
	v_add_f32_e32 v245, 1.0, v245
	v_add_f32_e32 v246, 1.0, v246
	v_add_f32_e32 v247, 1.0, v247
	v_rcp_f32_e32 v240, v240
	v_rcp_f32_e32 v241, v241
	v_rcp_f32_e32 v242, v242
	v_rcp_f32_e32 v243, v243
	v_rcp_f32_e32 v244, v244
	v_rcp_f32_e32 v245, v245
	v_rcp_f32_e32 v246, v246
	v_rcp_f32_e32 v247, v247
	s_nop 0
	v_cvt_pk_bf16_f32 v14, v240, v241
	v_cvt_pk_bf16_f32 v15, v242, v243
	v_cvt_pk_bf16_f32 v16, v244, v245
	v_cvt_pk_bf16_f32 v17, v246, v247
	global_store_dwordx4 v[234:235], v[14:17], off sc1
	v_cvt_f32_i32_e32 v6, v6
	v_cvt_f32_i32_e32 v7, v7
	v_cvt_f32_i32_e32 v8, v8
	v_cvt_f32_i32_e32 v9, v9
	v_cvt_f32_i32_e32 v2, v2
	v_cvt_f32_i32_e32 v3, v3
	v_cvt_f32_i32_e32 v4, v4
	v_cvt_f32_i32_e32 v5, v5
	v_pk_mul_f32 v[6:7], v[6:7], v[198:199] op_sel_hi:[1,0]
	v_pk_mul_f32 v[8:9], v[8:9], v[198:199] op_sel_hi:[1,0]
	v_pk_mul_f32 v[2:3], v[2:3], v[198:199] op_sel_hi:[1,0]
	v_pk_mul_f32 v[4:5], v[4:5], v[198:199] op_sel_hi:[1,0]
	v_pk_mul_f32 v[6:7], v[6:7], v[226:227]
	v_pk_mul_f32 v[8:9], v[8:9], v[228:229]
	v_pk_mul_f32 v[2:3], v[2:3], v[230:231]
	v_pk_mul_f32 v[4:5], v[4:5], v[232:233]
	v_mul_f32_e32 v240, 0xbfb8aa3b, v6
	v_mul_f32_e32 v241, 0xbfb8aa3b, v7
	v_mul_f32_e32 v242, 0xbfb8aa3b, v8
	v_mul_f32_e32 v243, 0xbfb8aa3b, v9
	v_mul_f32_e32 v244, 0xbfb8aa3b, v2
	v_mul_f32_e32 v245, 0xbfb8aa3b, v3
	v_mul_f32_e32 v246, 0xbfb8aa3b, v4
	v_mul_f32_e32 v247, 0xbfb8aa3b, v5
	v_exp_f32_e32 v240, v240
	v_exp_f32_e32 v241, v241
	v_exp_f32_e32 v242, v242
	v_exp_f32_e32 v243, v243
	v_exp_f32_e32 v244, v244
	v_exp_f32_e32 v245, v245
	v_exp_f32_e32 v246, v246
	v_exp_f32_e32 v247, v247
	v_add_f32_e32 v240, 1.0, v240
	v_add_f32_e32 v241, 1.0, v241
	v_add_f32_e32 v242, 1.0, v242
	v_add_f32_e32 v243, 1.0, v243
	v_add_f32_e32 v244, 1.0, v244
	v_add_f32_e32 v245, 1.0, v245
	v_add_f32_e32 v246, 1.0, v246
	v_add_f32_e32 v247, 1.0, v247
	v_rcp_f32_e32 v240, v240
	v_rcp_f32_e32 v241, v241
	v_rcp_f32_e32 v242, v242
	v_rcp_f32_e32 v243, v243
	v_rcp_f32_e32 v244, v244
	v_rcp_f32_e32 v245, v245
	v_rcp_f32_e32 v246, v246
	v_rcp_f32_e32 v247, v247
	s_nop 0
	v_cvt_pk_bf16_f32 v6, v240, v241
	v_cvt_pk_bf16_f32 v7, v242, v243
	v_cvt_pk_bf16_f32 v8, v244, v245
	v_cvt_pk_bf16_f32 v9, v246, v247
	global_store_dwordx4 v[236:237], v[6:9], off sc1
.Lfast_tail:
	s_andn2_b64 vcc, exec, s[8:9]
	s_mov_b64 s[8:9], -1
	s_cbranch_vccnz .LBB0_234
.Lpre_next:
	s_and_saveexec_b64 s[8:9], s[4:5]
	s_xor_b64 s[8:9], exec, s[8:9]
	v_lshl_add_u32 v2, s38, 8, v0
	v_ashrrev_i32_e32 v3, 31, v2
	s_movk_i32 s2, 0xfc00
	v_lshl_add_u64 v[2:3], v[2:3], 2, s[86:87]
	s_mov_b32 s3, -1
	v_lshl_add_u64 v[2:3], v[2:3], 0, s[2:3]
	s_lshl_b32 s2, s16, 8
	s_or_saveexec_b64 s[8:9], s[8:9]
	v_mov_b32_e32 v4, s2
	s_xor_b64 exec, exec, s[8:9]
	s_lshl_b32 s2, s16, 8
	v_or_b32_e32 v2, s2, v0
	v_ashrrev_i32_e32 v3, 31, v2
	v_lshl_add_u64 v[2:3], v[2:3], 2, s[84:85]
	v_mov_b32_e32 v4, s2
	s_or_b64 exec, exec, s[8:9]
	global_load_dword v18, v[2:3], off
	v_or_b32_sdwa v2, v4, v0 dst_sel:DWORD dst_unused:UNUSED_PAD src0_sel:DWORD src1_sel:BYTE_0
	v_readlane_b32 s40, v254, 7
	v_ashrrev_i32_e32 v3, 31, v2
	v_readlane_b32 s44, v254, 11
	v_readlane_b32 s45, v254, 12
	s_andn2_b64 vcc, exec, s[22:23]
	v_readlane_b32 s41, v254, 8
	v_lshl_add_u64 v[2:3], v[2:3], 2, s[44:45]
	global_load_dword v19, v[2:3], off
	v_readlane_b32 s42, v254, 9
	v_readlane_b32 s43, v254, 10
	v_readlane_b32 s46, v254, 13
	v_readlane_b32 s47, v254, 14
	v_readlane_b32 s48, v254, 15
	v_readlane_b32 s49, v254, 16
	v_readlane_b32 s50, v254, 17
	v_readlane_b32 s51, v254, 18
	v_readlane_b32 s52, v254, 19
	v_readlane_b32 s53, v254, 20
	v_readlane_b32 s54, v254, 21
	v_readlane_b32 s55, v254, 22
	s_cbranch_vccnz .LBB0_233
	s_barrier
	s_branch .LBB0_233
